# mixer A row sums as f32 VALU adds in the softmax section (issue slack there), no row-sum MFMAs in its pipe-bound MFMA section; mixer B keeps the 16x16x32 row sums
# baseline (speedup 1.0000x reference)
; #define ATT_PK4(P, BASE, OUT) do { u32x4 w = {cvtpk(P[BASE + 0], P[BASE + 1]), cvtpk(P[BASE + 2], P[BASE + 3]), cvtpk(P[BASE + 4], P[BASE + 5]), cvtpk(P[BASE + 6], P[BASE + 7])}; \
;     OUT = *reinterpret_cast<bf16x8*>(&w); } while (0)
; template <int DQK> __device__ __forceinline__ void qkt(f32x16& p0, f32x16& p1, const char* Ks, const bf16x8* qr, int r32, int hi) {
;   p0 = f32x16{}; p1 = f32x16{};
; #pragma unroll
;   for (int d0 = 0; d0 < DQK / 16; ++d0) { const int cb = (d0 * 16 + hi * 8) * 2;
;     const bf16x8 b0 = *reinterpret_cast<const bf16x8*>(Ks + kswz<DQK>(r32, cb));
;     const bf16x8 b1 = *reinterpret_cast<const bf16x8*>(Ks + kswz<DQK>(32 + r32, cb));
;     p0 = __builtin_amdgcn_mfma_f32_32x32x16_bf16(b0, qr[d0], p0, 0, 0, 0);
;     p1 = __builtin_amdgcn_mfma_f32_32x32x16_bf16(b1, qr[d0], p1, 0, 0, 0); }
; }
; __device__ __forceinline__ float softmax_shift(f32x16& p0, f32x16& p1, f32x16& negm, float pmax, bool first) {
;   asm volatile("s_nop 4" ::: "memory");
;   { auto rr = __builtin_amdgcn_permlane32_swap(__float_as_uint(pmax), __float_as_uint(pmax), false, false);
;     pmax = fmaxf(__uint_as_float(rr[0]), __uint_as_float(rr[1])); }
;   const float delta = first ? pmax : fmaxf(pmax, 0.f);
; #pragma unroll
;   for (int r = 0; r < 16; ++r) { p0[r] -= delta; p1[r] -= delta; negm[r] -= delta; }
;   return first ? 1.f : __builtin_amdgcn_exp2f(-delta);
; }
; __device__ __forceinline__ void softmax_exp_pack(f32x16& p0, f32x16& p1, bf16x8& pa0, bf16x8& pa1, bf16x8& pa2, bf16x8& pa3) {
; #pragma unroll
;   for (int r = 0; r < 16; ++r) { p0[r] = __builtin_amdgcn_exp2f(p0[r]); p1[r] = __builtin_amdgcn_exp2f(p1[r]); }
;     ...
;   ATT_PK4(p0, 0, pa0); ATT_PK4(p0, 8, pa1); ATT_PK4(p1, 0, pa2); ATT_PK4(p1, 8, pa3);
;     ...
; }
.LBB0_264:
	v_mul_u32_u24_e32 v18, 0x110, v213
	v_add3_u32 v69, 0, v184, v18
	ds_read_b128 v[18:21], v69 offset:49152
	v_mad_u32_u24 v188, v213, s54, 0
	v_add_u32_e32 v192, v188, v184
	ds_read_b128 v[34:37], v192 offset:57856
	ds_read_b128 v[70:73], v69 offset:49184
	ds_read_b128 v[74:77], v69 offset:49216
	s_and_b32 s4, s89, 0x3fffffc0
	s_lshl_b32 s4, s4, 2
	s_add_i32 s90, s4, 0
	s_add_i32 s90, s90, 0x23080
	s_waitcnt lgkmcnt(3)
	v_mfma_f32_32x32x16_bf16 v[18:33], v[18:21], v[136:139], 0
	s_mov_b32 s95, 1
	s_waitcnt lgkmcnt(2)
	v_mfma_f32_32x32x16_bf16 v[34:49], v[34:37], v[136:139], 0
	s_waitcnt lgkmcnt(1)
	v_mfma_f32_32x32x16_bf16 v[18:33], v[70:73], v[140:143], v[18:33]
	ds_read_b128 v[70:73], v69 offset:57888
	ds_read_b128 v[78:81], v69 offset:49376
	s_waitcnt lgkmcnt(1)
	v_mfma_f32_32x32x16_bf16 v[34:49], v[70:73], v[140:143], v[34:49]
	v_mfma_f32_32x32x16_bf16 v[18:33], v[74:77], v[144:147], v[18:33]
	ds_read_b128 v[70:73], v69 offset:57920
	ds_read_b128 v[74:77], v69 offset:57952
	s_waitcnt lgkmcnt(1)
	v_mfma_f32_32x32x16_bf16 v[34:49], v[70:73], v[144:147], v[34:49]
	ds_read_b128 v[70:73], v69 offset:49248
	ds_read_b128 v[82:85], v69 offset:49280
	s_waitcnt lgkmcnt(1)
	v_mfma_f32_32x32x16_bf16 v[18:33], v[70:73], v[148:151], v[18:33]
	v_mfma_f32_32x32x16_bf16 v[34:49], v[74:77], v[148:151], v[34:49]
	ds_read_b128 v[70:73], v69 offset:57984
	ds_read_b128 v[74:77], v69 offset:58016
	s_waitcnt lgkmcnt(2)
	v_mfma_f32_32x32x16_bf16 v[18:33], v[82:85], v[152:155], v[18:33]
	s_waitcnt lgkmcnt(1)
	v_mfma_f32_32x32x16_bf16 v[34:49], v[70:73], v[152:155], v[34:49]
	ds_read_b128 v[70:73], v69 offset:49312
	ds_read_b128 v[82:85], v69 offset:49344
	s_waitcnt lgkmcnt(1)
	v_mfma_f32_32x32x16_bf16 v[18:33], v[70:73], v[156:159], v[18:33]
	v_mfma_f32_32x32x16_bf16 v[34:49], v[74:77], v[156:159], v[34:49]
	ds_read_b128 v[70:73], v69 offset:58048
	ds_read_b128 v[74:77], v69 offset:58080
	v_and_b32_e32 v69, 63, v212
	s_waitcnt lgkmcnt(2)
	v_mfma_f32_32x32x16_bf16 v[18:33], v[82:85], v[160:163], v[18:33]
	s_waitcnt lgkmcnt(1)
	v_mfma_f32_32x32x16_bf16 v[34:49], v[70:73], v[160:163], v[34:49]
	v_lshlrev_b32_e32 v70, 3, v69
	v_lshlrev_b32_e32 v72, 4, v69
	v_lshlrev_b32_e32 v73, 1, v69
	v_and_b32_e32 v71, 24, v70
	v_and_b32_e32 v72, 0xc0, v72
	v_and_b32_e32 v73, 32, v73
	v_and_b32_e32 v70, 0x100, v70
	v_mfma_f32_32x32x16_bf16 v[18:33], v[78:81], v[164:167], v[18:33]
	s_waitcnt lgkmcnt(0)
	v_mfma_f32_32x32x16_bf16 v[34:49], v[74:77], v[164:167], v[34:49]
	s_barrier
	v_add3_u32 v71, 0, v71, v72
	v_add3_u32 v131, v71, v73, v70
	v_cmp_gt_u32_e64 s[4:5], 32, v69
	s_nop 8
	v_add_f32_e32 v69, 0, v34
	v_max3_f32 v70, v69, v18, v19
	v_max3_f32 v70, v70, v20, v21
	v_max3_f32 v70, v70, v22, v23
	v_max3_f32 v70, v70, v24, v25
	v_max3_f32 v70, v70, v26, v27
	v_max3_f32 v70, v70, v28, v29
	v_max3_f32 v70, v70, v30, v31
	v_max3_f32 v70, v70, v32, v33
	s_nop 4
	v_lshl_add_u32 v187, v213, 2, s90
	v_max3_f32 v69, v70, v35, v36
	v_max3_f32 v69, v69, v37, v38
	v_max3_f32 v69, v69, v39, v40
	v_max3_f32 v69, v69, v41, v42
	v_max3_f32 v69, v69, v43, v44
	v_max3_f32 v69, v69, v45, v46
	v_max3_f32 v69, v69, v47, v48
	v_max_f32 v69, v69, v49
	s_nop 0
	v_mov_b32_e32 v70, v69
	s_nop 1
	v_permlane32_swap_b32_e32 v69, v70
	v_max_f32_e32 v70, v70, v70
	v_max_f32_e32 v69, v69, v69
	v_max_f32_e32 v69, v69, v70
	v_sub_f32_e32 v18, v18, v69
	v_sub_f32_e32 v34, v34, v69
	v_sub_f32_e32 v19, v19, v69
	v_sub_f32_e32 v35, v35, v69
	v_sub_f32_e32 v20, v20, v69
	v_sub_f32_e32 v36, v36, v69
	v_sub_f32_e32 v21, v21, v69
	v_sub_f32_e32 v37, v37, v69
	v_sub_f32_e32 v22, v22, v69
	v_sub_f32_e32 v38, v38, v69
	v_sub_f32_e32 v23, v23, v69
	v_sub_f32_e32 v39, v39, v69
	v_sub_f32_e32 v24, v24, v69
	v_sub_f32_e32 v40, v40, v69
	v_sub_f32_e32 v25, v25, v69
	v_sub_f32_e32 v41, v41, v69
	v_sub_f32_e32 v26, v26, v69
	v_sub_f32_e32 v42, v42, v69
	v_sub_f32_e32 v27, v27, v69
	v_sub_f32_e32 v43, v43, v69
	v_sub_f32_e32 v28, v28, v69
	v_sub_f32_e32 v44, v44, v69
	v_sub_f32_e32 v29, v29, v69
	v_sub_f32_e32 v45, v45, v69
	v_sub_f32_e32 v30, v30, v69
	v_sub_f32_e32 v46, v46, v69
	v_sub_f32_e32 v31, v31, v69
	v_sub_f32_e32 v47, v47, v69
	v_sub_f32_e32 v32, v32, v69
	v_sub_f32_e32 v48, v48, v69
	v_sub_f32_e32 v33, v33, v69
	v_sub_f32_e32 v49, v49, v69
	v_exp_f32_e32 v18, v18
	v_exp_f32_e32 v34, v34
	v_exp_f32_e32 v19, v19
	v_exp_f32_e32 v35, v35
	v_exp_f32_e32 v20, v20
	v_exp_f32_e32 v36, v36
	v_exp_f32_e32 v21, v21
	v_exp_f32_e32 v37, v37
	v_exp_f32_e32 v22, v22
	v_exp_f32_e32 v38, v38
	v_exp_f32_e32 v23, v23
	v_exp_f32_e32 v39, v39
	v_exp_f32_e32 v24, v24
	v_exp_f32_e32 v40, v40
	v_exp_f32_e32 v25, v25
	v_exp_f32_e32 v41, v41
	v_exp_f32_e32 v26, v26
	v_exp_f32_e32 v42, v42
	v_exp_f32_e32 v27, v27
	v_exp_f32_e32 v43, v43
	v_exp_f32_e32 v28, v28
	v_exp_f32_e32 v44, v44
	v_exp_f32_e32 v29, v29
	v_exp_f32_e32 v45, v45
	v_exp_f32_e32 v30, v30
	v_exp_f32_e32 v46, v46
	v_exp_f32_e32 v31, v31
	v_exp_f32_e32 v47, v47
	v_exp_f32_e32 v32, v32
	v_exp_f32_e32 v48, v48
	v_exp_f32_e32 v33, v33
	v_exp_f32_e32 v49, v49
	v_mov_b32_e32 v240, 0
	v_mov_b32_e32 v241, 0
	v_add_f32_e32 v240, v240, v18
	v_add_f32_e32 v241, v241, v34
	v_add_f32_e32 v240, v240, v19
	v_add_f32_e32 v241, v241, v35
	v_add_f32_e32 v240, v240, v20
	v_add_f32_e32 v241, v241, v36
	v_add_f32_e32 v240, v240, v21
	v_add_f32_e32 v241, v241, v37
	v_add_f32_e32 v240, v240, v22
	v_add_f32_e32 v241, v241, v38
	v_add_f32_e32 v240, v240, v23
	v_add_f32_e32 v241, v241, v39
	v_add_f32_e32 v240, v240, v24
	v_add_f32_e32 v241, v241, v40
	v_add_f32_e32 v240, v240, v25
	v_add_f32_e32 v241, v241, v41
	v_add_f32_e32 v240, v240, v26
	v_add_f32_e32 v241, v241, v42
	v_add_f32_e32 v240, v240, v27
	v_add_f32_e32 v241, v241, v43
	v_add_f32_e32 v240, v240, v28
	v_add_f32_e32 v241, v241, v44
	v_add_f32_e32 v240, v240, v29
	v_add_f32_e32 v241, v241, v45
	v_add_f32_e32 v240, v240, v30
	v_add_f32_e32 v241, v241, v46
	v_add_f32_e32 v240, v240, v31
	v_add_f32_e32 v241, v241, v47
	v_add_f32_e32 v240, v240, v32
	v_add_f32_e32 v241, v241, v48
	v_add_f32_e32 v240, v240, v33
	v_add_f32_e32 v241, v241, v49
	v_sub_f32_e32 v82, 0, v69
	v_mov_b32_e32 v83, v82
	v_mov_b32_e32 v84, v82
	v_mov_b32_e32 v85, v82
	v_mov_b32_e32 v86, v82
	v_mov_b32_e32 v87, v82
	v_mov_b32_e32 v88, v82
	v_mov_b32_e32 v89, v82
	v_mov_b32_e32 v90, v82
	v_mov_b32_e32 v91, v82
	v_mov_b32_e32 v92, v82
	v_mov_b32_e32 v93, v82
	v_mov_b32_e32 v94, v82
	v_mov_b32_e32 v95, v82
	v_mov_b32_e32 v96, v82
	v_mov_b32_e32 v97, v82
	v_cvt_pk_bf16_f32 v98, v18, v19
	v_cvt_pk_bf16_f32 v99, v20, v21
	v_cvt_pk_bf16_f32 v100, v22, v23
	v_cvt_pk_bf16_f32 v101, v24, v25
	v_cvt_pk_bf16_f32 v102, v26, v27
	v_cvt_pk_bf16_f32 v103, v28, v29
	v_cvt_pk_bf16_f32 v104, v30, v31
	v_cvt_pk_bf16_f32 v105, v32, v33
	v_cvt_pk_bf16_f32 v106, v34, v35
	v_cvt_pk_bf16_f32 v107, v36, v37
	v_cvt_pk_bf16_f32 v108, v38, v39
	v_cvt_pk_bf16_f32 v109, v40, v41
	v_cvt_pk_bf16_f32 v110, v42, v43
	v_cvt_pk_bf16_f32 v111, v44, v45
	v_cvt_pk_bf16_f32 v112, v46, v47
	v_cvt_pk_bf16_f32 v113, v48, v49
	v_add_u32_e32 v18, 0x14800, v66
	s_waitcnt vmcnt(3)
; #define ATT_SBAR() __builtin_amdgcn_sched_barrier(0)
; __device__ __forceinline__ unsigned cvtpk(float lo, float hi) { f32x2_t v = {lo, hi}; bf16x2_t b = __builtin_convertvector(v, bf16x2_t); return __builtin_bit_cast(unsigned, b); }
; #define ATT_WRITE_K(so) do { *(bf16x8*)(K_lds + (so) + kswz<DQK>(kr, kc * 2)) = sk0; if constexpr (DQK == 128) *(bf16x8*)(K_lds + (so) + kswz<DQK>(32 + kr, kc * 2)) = sk1; } while (0)
; #define ATT_WRITE_V(so) do { *(bf16x8*)(V_lds + (so) + vst0) = sv0; *(bf16x8*)(V_lds + (so) + vst1) = sv1; } while (0)
; #define ATT_BAR() do { ATT_SBAR(); asm volatile("s_barrier" ::: "memory"); ATT_SBAR(); } while (0)
; #define ATT_SOFTMAX(first_) do { const float pm_ = softmax_rowmax(p0, p1); \
;     if (__builtin_expect((first_) || !__all(pm_ <= THRL), 0)) { const float al_ = softmax_shift(p0, p1, negm, pm_, (first_)); ATT_RESC(al_); } \
;     softmax_exp_pack(p0, p1, pa0, pa1, pa2, pa3); } while (0)
; #define ATT_VPAIR(buf, so, blk, ks) do { if constexpr (!(ABL & 8) && !(ABL & 32)) { buf[2 * (ks)] = vtr(vq0 + (so) + v_rd_off(blk, ks, 0)); buf[2 * (ks) + 1] = vtr(vq0 + (so) + v_rd_off(blk, ks, 1)); } } while (0)
;     ...
;   for (int t = 0; t + 1 < NT; ++t) {
;     if constexpr (ABL & 1) { u32x4 w0 = {cvtpk(p0[0], p0[1]), cvtpk(p0[2], p0[3]), cvtpk(p0[4], p0[5]), cvtpk(p0[6], p0[7])}, w1 = {cvtpk(p0[8], p0[9]), cvtpk(p0[10], p0[11]), cvtpk(p0[12], p0[13]), cvtpk(p0[14], p0[15])};
;         u32x4 w2 = {cvtpk(p1[0], p1[1]), cvtpk(p1[2], p1[3]), cvtpk(p1[4], p1[5]), cvtpk(p1[6], p1[7])}, w3 = {cvtpk(p1[8], p1[9]), cvtpk(p1[10], p1[11]), cvtpk(p1[12], p1[13]), cvtpk(p1[14], p1[15])};
;         pa0 = *reinterpret_cast<bf16x8*>(&w0); pa1 = *reinterpret_cast<bf16x8*>(&w1); pa2 = *reinterpret_cast<bf16x8*>(&w2); pa3 = *reinterpret_cast<bf16x8*>(&w3); }
;     else { ATT_SOFTMAX(t == 0); }
;     if constexpr (!(ABL & 4)) { ATT_WRITE_K(k2); ATT_WRITE_V(v1); }
;     ATT_SBAR();
; #pragma unroll
;     for (int ks = 0; ks < 4; ++ks) ATT_VPAIR(va, v0, 0, ks);
;     asm volatile("s_waitcnt lgkmcnt(8)" ::: "memory"); ATT_BAR();
	ds_write_b128 v18, v[50:53]
	s_waitcnt vmcnt(2)
	ds_write_b128 v18, v[54:57] offset:8704
	s_waitcnt vmcnt(1)
	ds_write_b128 v67, v[58:61] offset:16384
	s_waitcnt vmcnt(0)
	ds_write_b128 v68, v[62:65] offset:16384
	ds_read_b64_tr_b16 v[18:19], v131
	ds_read_b64_tr_b16 v[20:21], v131 offset:2048
	ds_read_b64_tr_b16 v[34:35], v131 offset:4096
	ds_read_b64_tr_b16 v[36:37], v131 offset:6144
	ds_read_b64_tr_b16 v[38:39], v131 offset:8192
	ds_read_b64_tr_b16 v[40:41], v131 offset:10240
	ds_read_b64_tr_b16 v[42:43], v131 offset:12288
	ds_read_b64_tr_b16 v[44:45], v131 offset:14336
	s_waitcnt lgkmcnt(8)
	s_barrier
	s_setprio 2
	s_waitcnt lgkmcnt(6)
	v_mfma_f32_32x32x16_bf16 v[18:33], v[98:101], v[18:21], 0
	ds_read_b64_tr_b16 v[46:47], v131 offset:512
	ds_read_b64_tr_b16 v[48:49], v131 offset:2560
	s_waitcnt lgkmcnt(6)
	v_mfma_f32_32x32x16_bf16 v[18:33], v[102:105], v[34:37], v[18:33]
	ds_read_b64_tr_b16 v[50:51], v131 offset:4608
	ds_read_b64_tr_b16 v[52:53], v131 offset:6656
	s_waitcnt lgkmcnt(6)
	v_mfma_f32_32x32x16_bf16 v[18:33], v[106:109], v[38:41], v[18:33]
	ds_read_b64_tr_b16 v[54:55], v131 offset:8704
	ds_read_b64_tr_b16 v[56:57], v131 offset:10752
	s_waitcnt lgkmcnt(6)
	v_mfma_f32_32x32x16_bf16 v[18:33], v[110:113], v[42:45], v[18:33]
	ds_read_b64_tr_b16 v[58:59], v131 offset:12800
	ds_read_b64_tr_b16 v[60:61], v131 offset:14848
	s_waitcnt lgkmcnt(6)
	v_mfma_f32_32x32x16_bf16 v[34:49], v[98:101], v[46:49], 0
	ds_read_b64_tr_b16 v[62:63], v131 offset:1024
	ds_read_b64_tr_b16 v[64:65], v131 offset:3072
	s_waitcnt lgkmcnt(6)
	v_mfma_f32_32x32x16_bf16 v[34:49], v[102:105], v[50:53], v[34:49]
	ds_read_b64_tr_b16 v[66:67], v131 offset:5120
	ds_read_b64_tr_b16 v[68:69], v131 offset:7168
	s_waitcnt lgkmcnt(6)
	v_mfma_f32_32x32x16_bf16 v[34:49], v[106:109], v[54:57], v[34:49]
	ds_read_b64_tr_b16 v[70:71], v131 offset:9216
	ds_read_b64_tr_b16 v[72:73], v131 offset:11264
	s_waitcnt lgkmcnt(6)
	v_mfma_f32_32x32x16_bf16 v[34:49], v[110:113], v[58:61], v[34:49]
	ds_read_b64_tr_b16 v[74:75], v131 offset:13312
	ds_read_b64_tr_b16 v[76:77], v131 offset:15360
	s_waitcnt lgkmcnt(6)
	v_mfma_f32_32x32x16_bf16 v[50:65], v[98:101], v[62:65], 0
	ds_read_b64_tr_b16 v[78:79], v131 offset:1536
	ds_read_b64_tr_b16 v[80:81], v131 offset:3584
	s_waitcnt lgkmcnt(6)
	v_mfma_f32_32x32x16_bf16 v[50:65], v[102:105], v[66:69], v[50:65]
	ds_read_b64_tr_b16 v[114:115], v131 offset:5632
	ds_read_b64_tr_b16 v[116:117], v131 offset:7680
	s_waitcnt lgkmcnt(6)
	v_mfma_f32_32x32x16_bf16 v[50:65], v[106:109], v[70:73], v[50:65]
	ds_read_b64_tr_b16 v[118:119], v131 offset:9728
	ds_read_b64_tr_b16 v[120:121], v131 offset:11776
	s_waitcnt lgkmcnt(6)
	v_mfma_f32_32x32x16_bf16 v[50:65], v[110:113], v[74:77], v[50:65]
	ds_read_b64_tr_b16 v[122:123], v131 offset:13824
	ds_read_b64_tr_b16 v[124:125], v131 offset:15872
	s_waitcnt lgkmcnt(6)
	v_mfma_f32_32x32x16_bf16 v[66:81], v[98:101], v[78:81], 0
	v_add_u32_e32 v193, 0xc000, v192
	ds_read_b128 v[126:129], v193 offset:17408
	s_waitcnt lgkmcnt(5)
	v_mfma_f32_32x32x16_bf16 v[66:81], v[102:105], v[114:117], v[66:81]
	ds_read_b128 v[168:171], v193 offset:26112
	s_waitcnt lgkmcnt(4)
	v_mfma_f32_32x32x16_bf16 v[66:81], v[106:109], v[118:121], v[66:81]
	ds_read_b128 v[172:175], v193 offset:17440
	s_waitcnt lgkmcnt(3)
	v_mfma_f32_32x32x16_bf16 v[66:81], v[110:113], v[122:125], v[66:81]
	ds_read_b128 v[176:179], v193 offset:26144
	ds_read_b128 v[180:183], v193 offset:17472
	ds_read_b128 v[194:197], v193 offset:26176
	ds_read_b128 v[198:201], v193 offset:17504
	ds_read_b128 v[212:215], v193 offset:26208
	s_waitcnt lgkmcnt(7)
	v_mfma_f32_32x32x16_bf16 v[98:113], v[126:129], v[136:139], v[82:97]
	ds_read_b128 v[216:219], v193 offset:17536
	v_mov_b64_e32 v[128:129], v[96:97]
	v_mov_b64_e32 v[126:127], v[94:95]
	v_mov_b64_e32 v[124:125], v[92:93]
	v_mov_b64_e32 v[122:123], v[90:91]
	v_mov_b64_e32 v[120:121], v[88:89]
	v_mov_b64_e32 v[118:119], v[86:87]
	v_mov_b64_e32 v[116:117], v[84:85]
	v_mov_b64_e32 v[114:115], v[82:83]
	ds_read_b128 v[220:223], v193 offset:26240
	s_waitcnt lgkmcnt(8)
	v_mfma_f32_32x32x16_bf16 v[114:129], v[168:171], v[136:139], v[114:129]
	s_waitcnt lgkmcnt(7)
	v_mfma_f32_32x32x16_bf16 v[98:113], v[172:175], v[140:143], v[98:113]
	ds_read_b128 v[168:171], v193 offset:17568
	s_waitcnt lgkmcnt(7)
	v_mfma_f32_32x32x16_bf16 v[114:129], v[176:179], v[140:143], v[114:129]
	ds_read_b128 v[172:175], v193 offset:26272
	s_waitcnt lgkmcnt(7)
	v_mfma_f32_32x32x16_bf16 v[98:113], v[180:183], v[144:147], v[98:113]
	ds_read_b128 v[176:179], v193 offset:17600
	s_waitcnt lgkmcnt(7)
	v_mfma_f32_32x32x16_bf16 v[114:129], v[194:197], v[144:147], v[114:129]
	ds_read_b128 v[180:183], v193 offset:26304
	s_waitcnt lgkmcnt(7)
	v_mfma_f32_32x32x16_bf16 v[98:113], v[198:201], v[148:151], v[98:113]
	ds_read_b128 v[194:197], v193 offset:17632
	s_waitcnt lgkmcnt(7)
	v_mfma_f32_32x32x16_bf16 v[114:129], v[212:215], v[148:151], v[114:129]
	ds_read_b128 v[198:201], v193 offset:26336
	s_waitcnt lgkmcnt(7)
	v_mfma_f32_32x32x16_bf16 v[98:113], v[216:219], v[152:155], v[98:113]
	s_waitcnt lgkmcnt(6)
	v_mfma_f32_32x32x16_bf16 v[114:129], v[220:223], v[152:155], v[114:129]
	s_waitcnt lgkmcnt(5)
	v_mfma_f32_32x32x16_bf16 v[98:113], v[168:171], v[156:159], v[98:113]
	s_waitcnt lgkmcnt(4)
	v_mfma_f32_32x32x16_bf16 v[114:129], v[172:175], v[156:159], v[114:129]
	s_waitcnt lgkmcnt(3)
	v_mfma_f32_32x32x16_bf16 v[98:113], v[176:179], v[160:163], v[98:113]
	s_waitcnt lgkmcnt(2)
	v_mfma_f32_32x32x16_bf16 v[114:129], v[180:183], v[160:163], v[114:129]
	s_waitcnt lgkmcnt(1)
	v_mfma_f32_32x32x16_bf16 v[98:113], v[194:197], v[164:167], v[98:113]
	s_waitcnt lgkmcnt(0)
	v_mfma_f32_32x32x16_bf16 v[114:129], v[198:201], v[164:167], v[114:129]
	s_setprio 0
	s_mov_b32 s14, s10
	s_mov_b32 s15, s11
	s_mov_b32 s96, 0x1c000
	buffer_load_dwordx4 v[224:227], v191, s[8:11], s59 offen
	buffer_load_dwordx4 v[228:231], v191, s[8:11], s96 offen
	buffer_load_dwordx4 v[232:235], v191, s[12:15], s57 offen
	buffer_load_dwordx4 v[236:239], v191, s[12:15], s58 offen
	s_barrier
	s_mov_b32 s93, 0x8000
	s_movk_i32 s15, 0x4000
	s_movk_i32 s94, 0x4400
	s_mov_b32 s92, 0
	s_mov_b32 s14, 0x8800
	s_mov_b32 s91, 0

; #define ATT_SBAR() __builtin_amdgcn_sched_barrier(0)
; __device__ __forceinline__ unsigned cvtpk(float lo, float hi) { f32x2_t v = {lo, hi}; bf16x2_t b = __builtin_convertvector(v, bf16x2_t); return __builtin_bit_cast(unsigned, b); }
; #define ATT_PK4(P, BASE, OUT) do { u32x4 w = {cvtpk(P[BASE + 0], P[BASE + 1]), cvtpk(P[BASE + 2], P[BASE + 3]), cvtpk(P[BASE + 4], P[BASE + 5]), cvtpk(P[BASE + 6], P[BASE + 7])}; \
;     OUT = *reinterpret_cast<bf16x8*>(&w); } while (0)
; #define ATT_WRITE_K(so) do { *(bf16x8*)(K_lds + (so) + kswz<DQK>(kr, kc * 2)) = sk0; if constexpr (DQK == 128) *(bf16x8*)(K_lds + (so) + kswz<DQK>(32 + kr, kc * 2)) = sk1; } while (0)
; #define ATT_WRITE_V(so) do { *(bf16x8*)(V_lds + (so) + vst0) = sv0; *(bf16x8*)(V_lds + (so) + vst1) = sv1; } while (0)
; #define ATT_BAR() do { ATT_SBAR(); asm volatile("s_barrier" ::: "memory"); ATT_SBAR(); } while (0)
; #define ATT_VPAIR(buf, so, blk, ks) do { if constexpr (!(ABL & 8) && !(ABL & 32)) { buf[2 * (ks)] = vtr(vq0 + (so) + v_rd_off(blk, ks, 0)); buf[2 * (ks) + 1] = vtr(vq0 + (so) + v_rd_off(blk, ks, 1)); } } while (0)
; __device__ __forceinline__ void softmax_exp_pack(f32x16& p0, f32x16& p1, bf16x8& pa0, bf16x8& pa1, bf16x8& pa2, bf16x8& pa3) {
; #pragma unroll
;   for (int r = 0; r < 16; ++r) { p0[r] = __builtin_amdgcn_exp2f(p0[r]); p1[r] = __builtin_amdgcn_exp2f(p1[r]); }
;     ...
;   ATT_PK4(p0, 0, pa0); ATT_PK4(p0, 8, pa1); ATT_PK4(p1, 0, pa2); ATT_PK4(p1, 8, pa3);
;     ...
; }
;     ...
;   for (int t = 0; t + 1 < NT; ++t) {
;     if constexpr (ABL & 1) { u32x4 w0 = {cvtpk(p0[0], p0[1]), cvtpk(p0[2], p0[3]), cvtpk(p0[4], p0[5]), cvtpk(p0[6], p0[7])}, w1 = {cvtpk(p0[8], p0[9]), cvtpk(p0[10], p0[11]), cvtpk(p0[12], p0[13]), cvtpk(p0[14], p0[15])};
;         u32x4 w2 = {cvtpk(p1[0], p1[1]), cvtpk(p1[2], p1[3]), cvtpk(p1[4], p1[5]), cvtpk(p1[6], p1[7])}, w3 = {cvtpk(p1[8], p1[9]), cvtpk(p1[10], p1[11]), cvtpk(p1[12], p1[13]), cvtpk(p1[14], p1[15])};
;         pa0 = *reinterpret_cast<bf16x8*>(&w0); pa1 = *reinterpret_cast<bf16x8*>(&w1); pa2 = *reinterpret_cast<bf16x8*>(&w2); pa3 = *reinterpret_cast<bf16x8*>(&w3); }
;     else { ATT_SOFTMAX(t == 0); }
;     if constexpr (!(ABL & 4)) { ATT_WRITE_K(k2); ATT_WRITE_V(v1); }
;     ATT_SBAR();
; #pragma unroll
;     for (int ks = 0; ks < 4; ++ks) ATT_VPAIR(va, v0, 0, ks);
;     asm volatile("s_waitcnt lgkmcnt(8)" ::: "memory"); ATT_BAR();
.LBB0_266:
	v_exp_f32_e32 v98, v98
	v_exp_f32_e32 v114, v114
	v_exp_f32_e32 v99, v99
	v_exp_f32_e32 v115, v115
	v_exp_f32_e32 v100, v100
	v_exp_f32_e32 v101, v101
	v_exp_f32_e32 v102, v102
	v_exp_f32_e32 v103, v103
	v_exp_f32_e32 v106, v106
	v_exp_f32_e32 v107, v107
	v_exp_f32_e32 v116, v116
	v_exp_f32_e32 v117, v117
	v_exp_f32_e32 v118, v118
	v_exp_f32_e32 v119, v119
	v_exp_f32_e32 v104, v104
	v_exp_f32_e32 v120, v120
	v_exp_f32_e32 v105, v105
	v_exp_f32_e32 v121, v121
	v_exp_f32_e32 v122, v122
	v_exp_f32_e32 v123, v123
	v_exp_f32_e32 v108, v108
	v_exp_f32_e32 v124, v124
	v_exp_f32_e32 v109, v109
	v_exp_f32_e32 v125, v125
	v_exp_f32_e32 v110, v110
	v_exp_f32_e32 v126, v126
	v_exp_f32_e32 v111, v111
	v_exp_f32_e32 v127, v127
	v_exp_f32_e32 v112, v112
	v_exp_f32_e32 v128, v128
	v_exp_f32_e32 v113, v113
	v_exp_f32_e32 v129, v129
	v_add_f32_e32 v240, v240, v98
	v_add_f32_e32 v241, v241, v114
	v_add_f32_e32 v240, v240, v99
	v_add_f32_e32 v241, v241, v115
	v_add_f32_e32 v240, v240, v100
	v_add_f32_e32 v241, v241, v101
	v_add_f32_e32 v240, v240, v102
	v_add_f32_e32 v241, v241, v103
	v_add_f32_e32 v240, v240, v106
	v_add_f32_e32 v241, v241, v107
	v_add_f32_e32 v240, v240, v116
	v_add_f32_e32 v241, v241, v117
	v_add_f32_e32 v240, v240, v118
	v_add_f32_e32 v241, v241, v119
	v_add_f32_e32 v240, v240, v104
	v_add_f32_e32 v241, v241, v120
	v_add_f32_e32 v240, v240, v105
	v_add_f32_e32 v241, v241, v121
	v_add_f32_e32 v240, v240, v122
	v_add_f32_e32 v241, v241, v123
	v_add_f32_e32 v240, v240, v108
	v_add_f32_e32 v241, v241, v124
	v_add_f32_e32 v240, v240, v109
	v_add_f32_e32 v241, v241, v125
	v_add_f32_e32 v240, v240, v110
	v_add_f32_e32 v241, v241, v126
	v_add_f32_e32 v240, v240, v111
	v_add_f32_e32 v241, v241, v127
	v_add_f32_e32 v240, v240, v112
	v_add_f32_e32 v241, v241, v128
	v_add_f32_e32 v240, v240, v113
	v_add_f32_e32 v241, v241, v129
	s_add_i32 s14, s92, 0
	v_cvt_pk_bf16_f32 v98, v98, v99
	v_cvt_pk_bf16_f32 v99, v100, v101
	v_cvt_pk_bf16_f32 v100, v102, v103
	v_cvt_pk_bf16_f32 v102, v106, v107
	v_cvt_pk_bf16_f32 v106, v114, v115
	v_add_u32_e32 v114, s14, v186
	s_add_i32 s14, s93, 0
	s_waitcnt vmcnt(3)
	ds_write_b128 v114, v[224:227] offset:49152
	s_waitcnt vmcnt(2)
	ds_write_b128 v114, v[228:231] offset:57856
	v_add_u32_e32 v114, s14, v189
	v_cvt_pk_bf16_f32 v101, v104, v105
	v_cvt_pk_bf16_f32 v103, v108, v109
	v_cvt_pk_bf16_f32 v104, v110, v111
	v_cvt_pk_bf16_f32 v105, v112, v113
	v_cvt_pk_bf16_f32 v107, v116, v117
	v_cvt_pk_bf16_f32 v108, v118, v119
	v_cvt_pk_bf16_f32 v109, v120, v121
	v_cvt_pk_bf16_f32 v110, v122, v123
	v_cvt_pk_bf16_f32 v111, v124, v125
	v_cvt_pk_bf16_f32 v112, v126, v127
	v_cvt_pk_bf16_f32 v113, v128, v129
	s_waitcnt vmcnt(1)
	ds_write_b128 v114, v[232:235]
	v_add_u32_e32 v114, s14, v190
	s_waitcnt vmcnt(0)
	ds_write_b128 v114, v[236:239]
	v_add_u32_e32 v172, s97, v131
	ds_read_b64_tr_b16 v[114:115], v172
	ds_read_b64_tr_b16 v[116:117], v172 offset:2048
	ds_read_b64_tr_b16 v[118:119], v172 offset:4096
	ds_read_b64_tr_b16 v[120:121], v172 offset:6144
	ds_read_b64_tr_b16 v[122:123], v172 offset:8192
	ds_read_b64_tr_b16 v[124:125], v172 offset:10240
	ds_read_b64_tr_b16 v[126:127], v172 offset:12288
	ds_read_b64_tr_b16 v[128:129], v172 offset:14336
	s_waitcnt lgkmcnt(8)
	s_barrier
	s_setprio 2
	s_waitcnt lgkmcnt(6)
	v_mfma_f32_32x32x16_bf16 v[18:33], v[98:101], v[114:117], v[18:33]
	ds_read_b64_tr_b16 v[168:169], v172 offset:512
	ds_read_b64_tr_b16 v[170:171], v172 offset:2560
	s_waitcnt lgkmcnt(6)
	v_mfma_f32_32x32x16_bf16 v[18:33], v[102:105], v[118:121], v[18:33]
	ds_read_b64_tr_b16 v[114:115], v172 offset:4608
	ds_read_b64_tr_b16 v[116:117], v172 offset:6656
	s_waitcnt lgkmcnt(6)
	v_mfma_f32_32x32x16_bf16 v[18:33], v[106:109], v[122:125], v[18:33]
	ds_read_b64_tr_b16 v[118:119], v172 offset:8704
	ds_read_b64_tr_b16 v[120:121], v172 offset:10752
	s_waitcnt lgkmcnt(6)
	v_mfma_f32_32x32x16_bf16 v[18:33], v[110:113], v[126:129], v[18:33]
	ds_read_b64_tr_b16 v[122:123], v172 offset:12800
	ds_read_b64_tr_b16 v[124:125], v172 offset:14848
	s_waitcnt lgkmcnt(6)
	v_mfma_f32_32x32x16_bf16 v[34:49], v[98:101], v[168:171], v[34:49]
	ds_read_b64_tr_b16 v[126:127], v172 offset:1024
	ds_read_b64_tr_b16 v[128:129], v172 offset:3072
	s_waitcnt lgkmcnt(6)
	v_mfma_f32_32x32x16_bf16 v[34:49], v[102:105], v[114:117], v[34:49]
	ds_read_b64_tr_b16 v[168:169], v172 offset:5120
	ds_read_b64_tr_b16 v[170:171], v172 offset:7168
	s_waitcnt lgkmcnt(6)
	v_mfma_f32_32x32x16_bf16 v[34:49], v[106:109], v[118:121], v[34:49]
	ds_read_b64_tr_b16 v[114:115], v172 offset:9216
	ds_read_b64_tr_b16 v[116:117], v172 offset:11264
	s_waitcnt lgkmcnt(6)
	v_mfma_f32_32x32x16_bf16 v[34:49], v[110:113], v[122:125], v[34:49]
	ds_read_b64_tr_b16 v[118:119], v172 offset:13312
	ds_read_b64_tr_b16 v[120:121], v172 offset:15360
	s_waitcnt lgkmcnt(6)
	v_mfma_f32_32x32x16_bf16 v[50:65], v[98:101], v[126:129], v[50:65]
	ds_read_b64_tr_b16 v[122:123], v172 offset:1536
	ds_read_b64_tr_b16 v[124:125], v172 offset:3584
	s_waitcnt lgkmcnt(6)
	v_mfma_f32_32x32x16_bf16 v[50:65], v[102:105], v[168:171], v[50:65]
	ds_read_b64_tr_b16 v[126:127], v172 offset:5632
	ds_read_b64_tr_b16 v[128:129], v172 offset:7680
	s_waitcnt lgkmcnt(6)
	v_mfma_f32_32x32x16_bf16 v[50:65], v[106:109], v[114:117], v[50:65]
	ds_read_b64_tr_b16 v[168:169], v172 offset:9728
	ds_read_b64_tr_b16 v[170:171], v172 offset:11776
	s_waitcnt lgkmcnt(6)
; #define ATT_SBAR() __builtin_amdgcn_sched_barrier(0)
; __device__ __forceinline__ unsigned cvtpk(float lo, float hi) { f32x2_t v = {lo, hi}; bf16x2_t b = __builtin_convertvector(v, bf16x2_t); return __builtin_bit_cast(unsigned, b); }
; #define ATT_LOAD_K(t) do { const unsigned so_ = (unsigned)(t) * (unsigned)(KVBLK * LDK * 2); sk0 = __builtin_bit_cast(bf16x8, __builtin_amdgcn_raw_buffer_load_b128(krs, koff, so_, 0)); \
;     if constexpr (DQK == 128) sk1 = __builtin_bit_cast(bf16x8, __builtin_amdgcn_raw_buffer_load_b128(krs, koff, so_ + (unsigned)(32 * LDK * 2), 0)); } while (0)
; #define ATT_LOAD_V(t) do { const unsigned so_ = (unsigned)(t) * (unsigned)(KVBLK * LDV * 2); sv0 = __builtin_bit_cast(bf16x8, __builtin_amdgcn_raw_buffer_load_b128(vrs, voff, so_, 0)); \
;     sv1 = __builtin_bit_cast(bf16x8, __builtin_amdgcn_raw_buffer_load_b128(vrs, voff, so_ + (unsigned)(32 * LDV * 2), 0)); } while (0)
; #define ATT_WRITE_K(so) do { *(bf16x8*)(K_lds + (so) + kswz<DQK>(kr, kc * 2)) = sk0; if constexpr (DQK == 128) *(bf16x8*)(K_lds + (so) + kswz<DQK>(32 + kr, kc * 2)) = sk1; } while (0)
;     ...
;   for (int t = 0; t + 1 < NT; ++t) {
;     if constexpr (ABL & 1) { u32x4 w0 = {cvtpk(p0[0], p0[1]), cvtpk(p0[2], p0[3]), cvtpk(p0[4], p0[5]), cvtpk(p0[6], p0[7])}, w1 = {cvtpk(p0[8], p0[9]), cvtpk(p0[10], p0[11]), cvtpk(p0[12], p0[13]), cvtpk(p0[14], p0[15])};
;         u32x4 w2 = {cvtpk(p1[0], p1[1]), cvtpk(p1[2], p1[3]), cvtpk(p1[4], p1[5]), cvtpk(p1[6], p1[7])}, w3 = {cvtpk(p1[8], p1[9]), cvtpk(p1[10], p1[11]), cvtpk(p1[12], p1[13]), cvtpk(p1[14], p1[15])};
;         pa0 = *reinterpret_cast<bf16x8*>(&w0); pa1 = *reinterpret_cast<bf16x8*>(&w1); pa2 = *reinterpret_cast<bf16x8*>(&w2); pa3 = *reinterpret_cast<bf16x8*>(&w3); }
;     else { ATT_SOFTMAX(t == 0); }
;     if constexpr (!(ABL & 4)) { ATT_WRITE_K(k2); ATT_WRITE_V(v1); }
;     ATT_SBAR();
; #pragma unroll
;     for (int ks = 0; ks < 4; ++ks) ATT_VPAIR(va, v0, 0, ks);
;     asm volatile("s_waitcnt lgkmcnt(8)" ::: "memory"); ATT_BAR();
;     ATT_XSECTION(true);
;     if constexpr (!(ABL & 4)) { const int tk = (t + 3 < NT) ? t + 3 : NT - 1, tv = (t + 2 < NT) ? t + 2 : NT - 1; ATT_LOAD_K(tk); ATT_LOAD_V(tv); }
;     ATT_BAR();
;     { const int tk_ = k0; k0 = k1; k1 = k2; k2 = tk_; const int tv_ = v0; v0 = v1; v1 = v2; v2 = tv_; }
	v_mfma_f32_32x32x16_bf16 v[50:65], v[110:113], v[118:121], v[50:65]
	ds_read_b64_tr_b16 v[114:115], v172 offset:13824
	ds_read_b64_tr_b16 v[116:117], v172 offset:15872
	s_waitcnt lgkmcnt(6)
	v_mfma_f32_32x32x16_bf16 v[66:81], v[98:101], v[122:125], v[66:81]
	v_add_u32_e32 v193, s36, v192
	ds_read_b128 v[118:121], v193 offset:49152
	s_waitcnt lgkmcnt(5)
	v_mfma_f32_32x32x16_bf16 v[66:81], v[102:105], v[126:129], v[66:81]
	ds_read_b128 v[172:175], v193 offset:57856
	s_waitcnt lgkmcnt(4)
	v_mfma_f32_32x32x16_bf16 v[66:81], v[106:109], v[168:171], v[66:81]
	ds_read_b128 v[176:179], v193 offset:49184
	s_waitcnt lgkmcnt(3)
	v_mfma_f32_32x32x16_bf16 v[66:81], v[110:113], v[114:117], v[66:81]
	ds_read_b128 v[168:171], v193 offset:57888
	ds_read_b128 v[180:183], v193 offset:49216
	ds_read_b128 v[194:197], v193 offset:57920
	ds_read_b128 v[198:201], v193 offset:49248
	ds_read_b128 v[212:215], v193 offset:57952
	s_waitcnt lgkmcnt(7)
	v_mfma_f32_32x32x16_bf16 v[98:113], v[118:121], v[136:139], v[82:97]
	ds_read_b128 v[216:219], v193 offset:49280
	s_waitcnt lgkmcnt(7)
	v_mfma_f32_32x32x16_bf16 v[114:129], v[172:175], v[136:139], v[82:97]
	ds_read_b128 v[220:223], v193 offset:57984
	s_waitcnt lgkmcnt(7)
	v_mfma_f32_32x32x16_bf16 v[98:113], v[176:179], v[140:143], v[98:113]
	ds_read_b128 v[172:175], v193 offset:49312
	s_waitcnt lgkmcnt(7)
	v_mfma_f32_32x32x16_bf16 v[114:129], v[168:171], v[140:143], v[114:129]
	ds_read_b128 v[176:179], v193 offset:58016
	s_waitcnt lgkmcnt(7)
	v_mfma_f32_32x32x16_bf16 v[98:113], v[180:183], v[144:147], v[98:113]
	ds_read_b128 v[168:171], v193 offset:49344
	s_waitcnt lgkmcnt(7)
	v_mfma_f32_32x32x16_bf16 v[114:129], v[194:197], v[144:147], v[114:129]
	ds_read_b128 v[180:183], v193 offset:58048
	s_waitcnt lgkmcnt(7)
	v_mfma_f32_32x32x16_bf16 v[98:113], v[198:201], v[148:151], v[98:113]
	ds_read_b128 v[194:197], v193 offset:49376
	s_waitcnt lgkmcnt(7)
	v_mfma_f32_32x32x16_bf16 v[114:129], v[212:215], v[148:151], v[114:129]
	ds_read_b128 v[198:201], v193 offset:58080
	s_waitcnt lgkmcnt(7)
	v_mfma_f32_32x32x16_bf16 v[98:113], v[216:219], v[152:155], v[98:113]
	s_min_u32 s14, s95, 0x7c
	s_lshl_b32 s14, s14, 15
	s_add_i32 s15, s14, 0x18000
	s_add_i32 s14, s14, 0x1c000
	buffer_load_dwordx4 v[224:227], v191, s[8:11], s15 offen
	s_waitcnt lgkmcnt(6)
	v_mfma_f32_32x32x16_bf16 v[114:129], v[220:223], v[152:155], v[114:129]
	buffer_load_dwordx4 v[228:231], v191, s[8:11], s14 offen
	s_waitcnt lgkmcnt(5)
	v_mfma_f32_32x32x16_bf16 v[98:113], v[172:175], v[156:159], v[98:113]
	s_add_i32 s18, s96, 0xffffc000
	s_mov_b32 s14, s10
	s_mov_b32 s15, s11
	buffer_load_dwordx4 v[232:235], v191, s[12:15], s18 offen
	s_waitcnt lgkmcnt(4)
	v_mfma_f32_32x32x16_bf16 v[114:129], v[176:179], v[156:159], v[114:129]
	buffer_load_dwordx4 v[236:239], v191, s[12:15], s96 offen
	s_waitcnt lgkmcnt(3)
	v_mfma_f32_32x32x16_bf16 v[98:113], v[168:171], v[160:163], v[98:113]
	s_waitcnt lgkmcnt(2)
	v_mfma_f32_32x32x16_bf16 v[114:129], v[180:183], v[160:163], v[114:129]
	s_waitcnt lgkmcnt(1)
	v_mfma_f32_32x32x16_bf16 v[98:113], v[194:197], v[164:167], v[98:113]
	s_waitcnt lgkmcnt(0)
	v_mfma_f32_32x32x16_bf16 v[114:129], v[198:201], v[164:167], v[114:129]
	s_setprio 0
	s_barrier
	s_add_i32 s96, s96, 0x8000
	s_add_i32 s95, s95, 1
	s_cmpk_eq_i32 s95, 0x7e
	s_cbranch_scc1 .LBB0_274
	s_mov_b32 s14, s92
	s_mov_b32 s92, s94
	s_mov_b32 s94, s36
	s_mov_b32 s15, s93
	s_mov_b32 s93, s91
	s_mov_b32 s91, s97
	s_branch .LBB0_265
.LBB0_268:
	v_mov_b32_e32 v194, v193
	s_nop 1
	v_permlane32_swap_b32_e32 v193, v194
	v_max3_f32 v193, v193, v194, 0
	v_exp_f32_e64 v194, -v193
	s_nop 4
	s_nop 0
	v_cmp_gt_f32_e32 vcc, 1.0, v194
	s_cbranch_vccz .LBB0_272
	v_mul_f32_e32 v240, v194, v240
	v_mul_f32_e32 v241, v194, v241
	s_and_saveexec_b64 s[14:15], s[4:5]
	ds_write_b32 v187, v194
	s_or_b64 exec, exec, s[14:15]
	s_waitcnt lgkmcnt(0)
	v_add_u32_e32 v216, s90, v184
	ds_read_b128 v[194:197], v216 offset:96
	ds_read_b128 v[198:201], v216 offset:64
	ds_read_b128 v[212:215], v216 offset:32
	ds_read_b128 v[216:219], v216
	s_waitcnt lgkmcnt(3)
	v_pk_mul_f32 v[30:31], v[30:31], v[194:195]
	s_waitcnt lgkmcnt(2)
	v_pk_mul_f32 v[26:27], v[26:27], v[198:199]
	s_waitcnt lgkmcnt(1)
	v_pk_mul_f32 v[22:23], v[22:23], v[212:213]
	v_pk_mul_f32 v[32:33], v[32:33], v[196:197]
	v_pk_mul_f32 v[28:29], v[28:29], v[200:201]
	v_pk_mul_f32 v[24:25], v[24:25], v[214:215]
	s_waitcnt lgkmcnt(0)
	v_pk_mul_f32 v[20:21], v[20:21], v[218:219]
	v_pk_mul_f32 v[18:19], v[18:19], v[216:217]
	v_pk_mul_f32 v[46:47], v[46:47], v[194:195]
	v_pk_mul_f32 v[42:43], v[42:43], v[198:199]
	v_pk_mul_f32 v[38:39], v[38:39], v[212:213]
	v_pk_mul_f32 v[48:49], v[48:49], v[196:197]
	v_pk_mul_f32 v[44:45], v[44:45], v[200:201]
	v_pk_mul_f32 v[40:41], v[40:41], v[214:215]
	v_pk_mul_f32 v[36:37], v[36:37], v[218:219]
	v_pk_mul_f32 v[34:35], v[34:35], v[216:217]
	v_pk_mul_f32 v[62:63], v[62:63], v[194:195]
	v_pk_mul_f32 v[58:59], v[58:59], v[198:199]
	v_pk_mul_f32 v[54:55], v[54:55], v[212:213]
	v_pk_mul_f32 v[64:65], v[64:65], v[196:197]
	v_pk_mul_f32 v[60:61], v[60:61], v[200:201]
	v_pk_mul_f32 v[56:57], v[56:57], v[214:215]
	v_pk_mul_f32 v[52:53], v[52:53], v[218:219]
	v_pk_mul_f32 v[50:51], v[50:51], v[216:217]
	v_pk_mul_f32 v[78:79], v[78:79], v[194:195]
	v_pk_mul_f32 v[74:75], v[74:75], v[198:199]
	v_pk_mul_f32 v[70:71], v[70:71], v[212:213]
	v_pk_mul_f32 v[80:81], v[80:81], v[196:197]
	v_pk_mul_f32 v[76:77], v[76:77], v[200:201]
	v_pk_mul_f32 v[72:73], v[72:73], v[214:215]
	v_pk_mul_f32 v[68:69], v[68:69], v[218:219]
	v_pk_mul_f32 v[66:67], v[66:67], v[216:217]

; #define ATT_SBAR() __builtin_amdgcn_sched_barrier(0)
; __device__ __forceinline__ unsigned cvtpk(float lo, float hi) { f32x2_t v = {lo, hi}; bf16x2_t b = __builtin_convertvector(v, bf16x2_t); return __builtin_bit_cast(unsigned, b); }
; #define ATT_PK4(P, BASE, OUT) do { u32x4 w = {cvtpk(P[BASE + 0], P[BASE + 1]), cvtpk(P[BASE + 2], P[BASE + 3]), cvtpk(P[BASE + 4], P[BASE + 5]), cvtpk(P[BASE + 6], P[BASE + 7])}; \
;     OUT = *reinterpret_cast<bf16x8*>(&w); } while (0)
; #define ATT_WRITE_K(so) do { *(bf16x8*)(K_lds + (so) + kswz<DQK>(kr, kc * 2)) = sk0; if constexpr (DQK == 128) *(bf16x8*)(K_lds + (so) + kswz<DQK>(32 + kr, kc * 2)) = sk1; } while (0)
; #define ATT_WRITE_V(so) do { *(bf16x8*)(V_lds + (so) + vst0) = sv0; *(bf16x8*)(V_lds + (so) + vst1) = sv1; } while (0)
; #define ATT_BAR() do { ATT_SBAR(); asm volatile("s_barrier" ::: "memory"); ATT_SBAR(); } while (0)
; #define ATT_VPAIR(buf, so, blk, ks) do { if constexpr (!(ABL & 8) && !(ABL & 32)) { buf[2 * (ks)] = vtr(vq0 + (so) + v_rd_off(blk, ks, 0)); buf[2 * (ks) + 1] = vtr(vq0 + (so) + v_rd_off(blk, ks, 1)); } } while (0)
; __device__ __forceinline__ void softmax_exp_pack(f32x16& p0, f32x16& p1, bf16x8& pa0, bf16x8& pa1, bf16x8& pa2, bf16x8& pa3) {
; #pragma unroll
;   for (int r = 0; r < 16; ++r) { p0[r] = __builtin_amdgcn_exp2f(p0[r]); p1[r] = __builtin_amdgcn_exp2f(p1[r]); }
;     ...
;   ATT_PK4(p0, 0, pa0); ATT_PK4(p0, 8, pa1); ATT_PK4(p1, 0, pa2); ATT_PK4(p1, 8, pa3);
;     ...
; }
;     ...
;   for (int t = 0; t + 1 < NT; ++t) {
;     if constexpr (ABL & 1) { u32x4 w0 = {cvtpk(p0[0], p0[1]), cvtpk(p0[2], p0[3]), cvtpk(p0[4], p0[5]), cvtpk(p0[6], p0[7])}, w1 = {cvtpk(p0[8], p0[9]), cvtpk(p0[10], p0[11]), cvtpk(p0[12], p0[13]), cvtpk(p0[14], p0[15])};
;         u32x4 w2 = {cvtpk(p1[0], p1[1]), cvtpk(p1[2], p1[3]), cvtpk(p1[4], p1[5]), cvtpk(p1[6], p1[7])}, w3 = {cvtpk(p1[8], p1[9]), cvtpk(p1[10], p1[11]), cvtpk(p1[12], p1[13]), cvtpk(p1[14], p1[15])};
;         pa0 = *reinterpret_cast<bf16x8*>(&w0); pa1 = *reinterpret_cast<bf16x8*>(&w1); pa2 = *reinterpret_cast<bf16x8*>(&w2); pa3 = *reinterpret_cast<bf16x8*>(&w3); }
;     else { ATT_SOFTMAX(t == 0); }
;     if constexpr (!(ABL & 4)) { ATT_WRITE_K(k2); ATT_WRITE_V(v1); }
;     ATT_SBAR();
; #pragma unroll
;     for (int ks = 0; ks < 4; ++ks) ATT_VPAIR(va, v0, 0, ks);
;     asm volatile("s_waitcnt lgkmcnt(8)" ::: "memory"); ATT_BAR();
.LBB0_275:
	v_exp_f32_e32 v98, v98
	v_exp_f32_e32 v114, v114
	v_exp_f32_e32 v99, v99
	v_exp_f32_e32 v115, v115
	v_exp_f32_e32 v100, v100
	v_exp_f32_e32 v101, v101
	v_exp_f32_e32 v102, v102
	v_exp_f32_e32 v103, v103
	v_exp_f32_e32 v106, v106
	v_exp_f32_e32 v107, v107
	v_exp_f32_e32 v116, v116
	v_exp_f32_e32 v117, v117
	v_exp_f32_e32 v118, v118
	v_exp_f32_e32 v119, v119
	v_exp_f32_e32 v104, v104
	v_exp_f32_e32 v120, v120
	v_exp_f32_e32 v105, v105
	v_exp_f32_e32 v121, v121
	v_exp_f32_e32 v122, v122
	v_exp_f32_e32 v123, v123
	v_exp_f32_e32 v108, v108
	v_exp_f32_e32 v124, v124
	v_exp_f32_e32 v109, v109
	v_exp_f32_e32 v125, v125
	v_exp_f32_e32 v110, v110
	v_exp_f32_e32 v126, v126
	v_exp_f32_e32 v111, v111
	v_exp_f32_e32 v127, v127
	v_exp_f32_e32 v112, v112
	v_exp_f32_e32 v128, v128
	v_exp_f32_e32 v113, v113
	v_exp_f32_e32 v129, v129
	v_add_f32_e32 v240, v240, v98
	v_add_f32_e32 v241, v241, v114
	v_add_f32_e32 v240, v240, v99
	v_add_f32_e32 v241, v241, v115
	v_add_f32_e32 v240, v240, v100
	v_add_f32_e32 v241, v241, v101
	v_add_f32_e32 v240, v240, v102
	v_add_f32_e32 v241, v241, v103
	v_add_f32_e32 v240, v240, v106
	v_add_f32_e32 v241, v241, v107
	v_add_f32_e32 v240, v240, v116
	v_add_f32_e32 v241, v241, v117
	v_add_f32_e32 v240, v240, v118
	v_add_f32_e32 v241, v241, v119
	v_add_f32_e32 v240, v240, v104
	v_add_f32_e32 v241, v241, v120
	v_add_f32_e32 v240, v240, v105
	v_add_f32_e32 v241, v241, v121
	v_add_f32_e32 v240, v240, v122
	v_add_f32_e32 v241, v241, v123
	v_add_f32_e32 v240, v240, v108
	v_add_f32_e32 v241, v241, v124
	v_add_f32_e32 v240, v240, v109
	v_add_f32_e32 v241, v241, v125
	v_add_f32_e32 v240, v240, v110
	v_add_f32_e32 v241, v241, v126
	v_add_f32_e32 v240, v240, v111
	v_add_f32_e32 v241, v241, v127
	v_add_f32_e32 v240, v240, v112
	v_add_f32_e32 v241, v241, v128
	v_add_f32_e32 v240, v240, v113
	v_add_f32_e32 v241, v241, v129
	s_add_i32 s8, s94, 0
	v_cvt_pk_bf16_f32 v98, v98, v99
	v_cvt_pk_bf16_f32 v99, v100, v101
	v_cvt_pk_bf16_f32 v100, v102, v103
	v_cvt_pk_bf16_f32 v102, v106, v107
	v_cvt_pk_bf16_f32 v106, v114, v115
	v_add_u32_e32 v114, s8, v186
	s_add_i32 s8, s91, 0
	s_waitcnt vmcnt(3)
	ds_write_b128 v114, v[224:227] offset:49152
	s_waitcnt vmcnt(2)
	ds_write_b128 v114, v[228:231] offset:57856
	v_add_u32_e32 v114, s8, v189
	v_cvt_pk_bf16_f32 v101, v104, v105
	v_cvt_pk_bf16_f32 v103, v108, v109
	v_cvt_pk_bf16_f32 v104, v110, v111
	v_cvt_pk_bf16_f32 v105, v112, v113
	v_cvt_pk_bf16_f32 v107, v116, v117
	v_cvt_pk_bf16_f32 v108, v118, v119
	v_cvt_pk_bf16_f32 v109, v120, v121
	v_cvt_pk_bf16_f32 v110, v122, v123
	v_cvt_pk_bf16_f32 v111, v124, v125
	v_cvt_pk_bf16_f32 v112, v126, v127
	v_cvt_pk_bf16_f32 v113, v128, v129
	s_waitcnt vmcnt(1)
	ds_write_b128 v114, v[232:235]
	v_add_u32_e32 v114, s8, v190
	s_waitcnt vmcnt(0)
	ds_write_b128 v114, v[236:239]
	v_add_u32_e32 v172, s93, v131
	ds_read_b64_tr_b16 v[114:115], v172
	ds_read_b64_tr_b16 v[116:117], v172 offset:2048
	ds_read_b64_tr_b16 v[118:119], v172 offset:4096
	ds_read_b64_tr_b16 v[120:121], v172 offset:6144
	ds_read_b64_tr_b16 v[122:123], v172 offset:8192
	ds_read_b64_tr_b16 v[124:125], v172 offset:10240
	ds_read_b64_tr_b16 v[126:127], v172 offset:12288
	ds_read_b64_tr_b16 v[128:129], v172 offset:14336
	s_waitcnt lgkmcnt(8)
	s_barrier
	s_setprio 2
	s_waitcnt lgkmcnt(6)
	v_mfma_f32_32x32x16_bf16 v[18:33], v[98:101], v[114:117], v[18:33]
	ds_read_b64_tr_b16 v[168:169], v172 offset:512
	ds_read_b64_tr_b16 v[170:171], v172 offset:2560
	s_waitcnt lgkmcnt(6)
	v_mfma_f32_32x32x16_bf16 v[18:33], v[102:105], v[118:121], v[18:33]
	ds_read_b64_tr_b16 v[114:115], v172 offset:4608
	ds_read_b64_tr_b16 v[116:117], v172 offset:6656
	s_waitcnt lgkmcnt(6)
	v_mfma_f32_32x32x16_bf16 v[18:33], v[106:109], v[122:125], v[18:33]
	ds_read_b64_tr_b16 v[118:119], v172 offset:8704
	ds_read_b64_tr_b16 v[120:121], v172 offset:10752
	s_waitcnt lgkmcnt(6)
	v_mfma_f32_32x32x16_bf16 v[18:33], v[110:113], v[126:129], v[18:33]
	ds_read_b64_tr_b16 v[122:123], v172 offset:12800
	ds_read_b64_tr_b16 v[124:125], v172 offset:14848
	s_waitcnt lgkmcnt(6)
	v_mfma_f32_32x32x16_bf16 v[34:49], v[98:101], v[168:171], v[34:49]
	ds_read_b64_tr_b16 v[126:127], v172 offset:1024
	ds_read_b64_tr_b16 v[128:129], v172 offset:3072
	s_waitcnt lgkmcnt(6)
	v_mfma_f32_32x32x16_bf16 v[34:49], v[102:105], v[114:117], v[34:49]
	ds_read_b64_tr_b16 v[168:169], v172 offset:5120
	ds_read_b64_tr_b16 v[170:171], v172 offset:7168
	s_waitcnt lgkmcnt(6)
	v_mfma_f32_32x32x16_bf16 v[34:49], v[106:109], v[118:121], v[34:49]
	ds_read_b64_tr_b16 v[114:115], v172 offset:9216
	ds_read_b64_tr_b16 v[116:117], v172 offset:11264
	s_waitcnt lgkmcnt(6)
	v_mfma_f32_32x32x16_bf16 v[34:49], v[110:113], v[122:125], v[34:49]
	ds_read_b64_tr_b16 v[118:119], v172 offset:13312
	ds_read_b64_tr_b16 v[120:121], v172 offset:15360
	s_waitcnt lgkmcnt(6)
	v_mfma_f32_32x32x16_bf16 v[50:65], v[98:101], v[126:129], v[50:65]
	ds_read_b64_tr_b16 v[122:123], v172 offset:1536
	ds_read_b64_tr_b16 v[124:125], v172 offset:3584
	s_waitcnt lgkmcnt(6)
	v_mfma_f32_32x32x16_bf16 v[50:65], v[102:105], v[168:171], v[50:65]
	ds_read_b64_tr_b16 v[126:127], v172 offset:5632
	ds_read_b64_tr_b16 v[128:129], v172 offset:7680
	s_waitcnt lgkmcnt(6)
	v_mfma_f32_32x32x16_bf16 v[50:65], v[106:109], v[114:117], v[50:65]
	ds_read_b64_tr_b16 v[168:169], v172 offset:9728
	ds_read_b64_tr_b16 v[170:171], v172 offset:11776
	s_waitcnt lgkmcnt(6)
	v_mfma_f32_32x32x16_bf16 v[50:65], v[110:113], v[118:121], v[50:65]
	ds_read_b64_tr_b16 v[114:115], v172 offset:13824
	ds_read_b64_tr_b16 v[116:117], v172 offset:15872
	s_waitcnt lgkmcnt(6)
; #define ATT_SBAR() __builtin_amdgcn_sched_barrier(0)
; __device__ __forceinline__ unsigned cvtpk(float lo, float hi) { f32x2_t v = {lo, hi}; bf16x2_t b = __builtin_convertvector(v, bf16x2_t); return __builtin_bit_cast(unsigned, b); }
; #define ATT_LOAD_K(t) do { const unsigned so_ = (unsigned)(t) * (unsigned)(KVBLK * LDK * 2); sk0 = __builtin_bit_cast(bf16x8, __builtin_amdgcn_raw_buffer_load_b128(krs, koff, so_, 0)); \
;     if constexpr (DQK == 128) sk1 = __builtin_bit_cast(bf16x8, __builtin_amdgcn_raw_buffer_load_b128(krs, koff, so_ + (unsigned)(32 * LDK * 2), 0)); } while (0)
; #define ATT_LOAD_V(t) do { const unsigned so_ = (unsigned)(t) * (unsigned)(KVBLK * LDV * 2); sv0 = __builtin_bit_cast(bf16x8, __builtin_amdgcn_raw_buffer_load_b128(vrs, voff, so_, 0)); \
;     sv1 = __builtin_bit_cast(bf16x8, __builtin_amdgcn_raw_buffer_load_b128(vrs, voff, so_ + (unsigned)(32 * LDV * 2), 0)); } while (0)
;     ...
;   for (int t = 0; t + 1 < NT; ++t) {
;     if constexpr (ABL & 1) { u32x4 w0 = {cvtpk(p0[0], p0[1]), cvtpk(p0[2], p0[3]), cvtpk(p0[4], p0[5]), cvtpk(p0[6], p0[7])}, w1 = {cvtpk(p0[8], p0[9]), cvtpk(p0[10], p0[11]), cvtpk(p0[12], p0[13]), cvtpk(p0[14], p0[15])};
;         u32x4 w2 = {cvtpk(p1[0], p1[1]), cvtpk(p1[2], p1[3]), cvtpk(p1[4], p1[5]), cvtpk(p1[6], p1[7])}, w3 = {cvtpk(p1[8], p1[9]), cvtpk(p1[10], p1[11]), cvtpk(p1[12], p1[13]), cvtpk(p1[14], p1[15])};
;         pa0 = *reinterpret_cast<bf16x8*>(&w0); pa1 = *reinterpret_cast<bf16x8*>(&w1); pa2 = *reinterpret_cast<bf16x8*>(&w2); pa3 = *reinterpret_cast<bf16x8*>(&w3); }
;     else { ATT_SOFTMAX(t == 0); }
;     if constexpr (!(ABL & 4)) { ATT_WRITE_K(k2); ATT_WRITE_V(v1); }
;     ATT_SBAR();
; #pragma unroll
;     for (int ks = 0; ks < 4; ++ks) ATT_VPAIR(va, v0, 0, ks);
;     asm volatile("s_waitcnt lgkmcnt(8)" ::: "memory"); ATT_BAR();
;     ATT_XSECTION(true);
;     if constexpr (!(ABL & 4)) { const int tk = (t + 3 < NT) ? t + 3 : NT - 1, tv = (t + 2 < NT) ? t + 2 : NT - 1; ATT_LOAD_K(tk); ATT_LOAD_V(tv); }
;     ATT_BAR();
;     { const int tk_ = k0; k0 = k1; k1 = k2; k2 = tk_; const int tv_ = v0; v0 = v1; v1 = v2; v2 = tv_; }
;   }
;   ATT_SOFTMAX(false);
; #pragma unroll
;   for (int ks = 0; ks < 4; ++ks) ATT_VPAIR(va, v0, 0, ks);
;   asm volatile("s_waitcnt lgkmcnt(0)" ::: "memory"); ATT_BAR();
;   ATT_XSECTION(false);
	v_mfma_f32_32x32x16_bf16 v[66:81], v[98:101], v[122:125], v[66:81]
	v_add3_u32 v186, v188, s92, v184
	ds_read_b128 v[118:121], v186 offset:49152
	s_waitcnt lgkmcnt(5)
	v_mfma_f32_32x32x16_bf16 v[66:81], v[102:105], v[126:129], v[66:81]
	ds_read_b128 v[122:125], v186 offset:57856
	s_waitcnt lgkmcnt(4)
	v_mfma_f32_32x32x16_bf16 v[66:81], v[106:109], v[168:171], v[66:81]
	ds_read_b128 v[126:129], v186 offset:49184
	s_waitcnt lgkmcnt(3)
	v_mfma_f32_32x32x16_bf16 v[66:81], v[110:113], v[114:117], v[66:81]
	ds_read_b128 v[168:171], v186 offset:57888
	ds_read_b128 v[114:117], v186 offset:49216
	ds_read_b128 v[172:175], v186 offset:57920
	ds_read_b128 v[176:179], v186 offset:49248
	ds_read_b128 v[180:183], v186 offset:57952
	s_waitcnt lgkmcnt(7)
	v_mfma_f32_32x32x16_bf16 v[98:113], v[118:121], v[136:139], v[82:97]
	ds_read_b128 v[188:191], v186 offset:49280
	s_waitcnt lgkmcnt(7)
	v_mfma_f32_32x32x16_bf16 v[82:97], v[122:125], v[136:139], v[82:97]
	ds_read_b128 v[118:121], v186 offset:57984
	s_waitcnt lgkmcnt(7)
	v_mfma_f32_32x32x16_bf16 v[98:113], v[126:129], v[140:143], v[98:113]
	ds_read_b128 v[122:125], v186 offset:49312
	s_waitcnt lgkmcnt(7)
	v_mfma_f32_32x32x16_bf16 v[82:97], v[168:171], v[140:143], v[82:97]
	ds_read_b128 v[126:129], v186 offset:58016
	s_waitcnt lgkmcnt(7)
	v_mfma_f32_32x32x16_bf16 v[98:113], v[114:117], v[144:147], v[98:113]
	ds_read_b128 v[136:139], v186 offset:49344
	s_waitcnt lgkmcnt(7)
	v_mfma_f32_32x32x16_bf16 v[82:97], v[172:175], v[144:147], v[82:97]
	ds_read_b128 v[114:117], v186 offset:58048
	s_waitcnt lgkmcnt(7)
	v_mfma_f32_32x32x16_bf16 v[98:113], v[176:179], v[148:151], v[98:113]
	ds_read_b128 v[140:143], v186 offset:49376
	s_waitcnt lgkmcnt(7)
	v_mfma_f32_32x32x16_bf16 v[82:97], v[180:183], v[148:151], v[82:97]
	ds_read_b128 v[144:147], v186 offset:58080
	s_waitcnt lgkmcnt(7)
	v_mfma_f32_32x32x16_bf16 v[98:113], v[188:191], v[152:155], v[98:113]
	s_waitcnt lgkmcnt(6)
	v_mfma_f32_32x32x16_bf16 v[82:97], v[118:121], v[152:155], v[82:97]
	s_waitcnt lgkmcnt(5)
	v_mfma_f32_32x32x16_bf16 v[98:113], v[122:125], v[156:159], v[98:113]
	s_waitcnt lgkmcnt(4)
	v_mfma_f32_32x32x16_bf16 v[82:97], v[126:129], v[156:159], v[82:97]
	s_waitcnt lgkmcnt(3)
	v_mfma_f32_32x32x16_bf16 v[98:113], v[136:139], v[160:163], v[98:113]
	s_waitcnt lgkmcnt(2)
	v_mfma_f32_32x32x16_bf16 v[82:97], v[114:117], v[160:163], v[82:97]
	s_waitcnt lgkmcnt(1)
	v_mfma_f32_32x32x16_bf16 v[98:113], v[140:143], v[164:167], v[98:113]
	s_waitcnt lgkmcnt(0)
	v_mfma_f32_32x32x16_bf16 v[82:97], v[144:147], v[164:167], v[82:97]
	s_setprio 0
	s_barrier
	s_nop 10
	v_add_f32_e32 v114, 0, v82
	v_max3_f32 v115, v114, v98, v99
	v_max3_f32 v115, v115, v100, v101
	v_max3_f32 v115, v115, v102, v103
	v_max3_f32 v115, v115, v104, v105
	v_max3_f32 v115, v115, v106, v107
	v_max3_f32 v115, v115, v108, v109
	v_max3_f32 v115, v115, v110, v111
	v_max3_f32 v115, v115, v112, v113
	s_nop 0
	v_max3_f32 v114, v115, v83, v84
	v_max3_f32 v114, v114, v85, v86
	v_max3_f32 v114, v114, v87, v88
	v_max3_f32 v114, v114, v89, v90
	v_max3_f32 v114, v114, v91, v92
	v_max3_f32 v114, v114, v93, v94
	v_max3_f32 v114, v114, v95, v96
	v_max_f32 v114, v114, v97
	s_nop 0
	v_cmp_ge_f32_e32 vcc, s60, v114
	s_cmp_lg_u64 vcc, exec
	s_cbranch_scc1 .LBB0_314
.LBB0_276:
	v_exp_f32_e32 v98, v98
	v_exp_f32_e32 v114, v82
	v_exp_f32_e32 v82, v99
	v_exp_f32_e32 v99, v83
	v_exp_f32_e32 v83, v100
	v_exp_f32_e32 v100, v84
	v_exp_f32_e32 v84, v101
	v_exp_f32_e32 v101, v85
	v_exp_f32_e32 v85, v102
	v_exp_f32_e32 v102, v86
	v_exp_f32_e32 v86, v103
	v_exp_f32_e32 v103, v87
	v_exp_f32_e32 v87, v104
	v_exp_f32_e32 v104, v88
	v_exp_f32_e32 v88, v105
	v_exp_f32_e32 v105, v89
	v_exp_f32_e32 v89, v106
	v_exp_f32_e32 v106, v90
	v_exp_f32_e32 v90, v107
	v_exp_f32_e32 v107, v91
	v_exp_f32_e32 v91, v108
	v_exp_f32_e32 v108, v92
	v_exp_f32_e32 v92, v109
	v_exp_f32_e32 v109, v93
	v_exp_f32_e32 v93, v110
	v_exp_f32_e32 v110, v94
	v_exp_f32_e32 v94, v111
	v_exp_f32_e32 v111, v95
	v_exp_f32_e32 v95, v112
	v_exp_f32_e32 v112, v96
	v_exp_f32_e32 v96, v113
	v_exp_f32_e32 v97, v97
	v_add_f32_e32 v240, v240, v98
	v_add_f32_e32 v241, v241, v114
	v_add_f32_e32 v240, v240, v82
	v_add_f32_e32 v241, v241, v99
	v_add_f32_e32 v240, v240, v83
	v_add_f32_e32 v241, v241, v100
	v_add_f32_e32 v240, v240, v84
	v_add_f32_e32 v241, v241, v101
	v_add_f32_e32 v240, v240, v85
	v_add_f32_e32 v241, v241, v102
	v_add_f32_e32 v240, v240, v86
	v_add_f32_e32 v241, v241, v103
	v_add_f32_e32 v240, v240, v87
	v_add_f32_e32 v241, v241, v104
	v_add_f32_e32 v240, v240, v88
	v_add_f32_e32 v241, v241, v105
	v_add_f32_e32 v240, v240, v89
	v_add_f32_e32 v241, v241, v106
	v_add_f32_e32 v240, v240, v90
	v_add_f32_e32 v241, v241, v107
	v_add_f32_e32 v240, v240, v91
	v_add_f32_e32 v241, v241, v108
	v_add_f32_e32 v240, v240, v92
	v_add_f32_e32 v241, v241, v109
	v_add_f32_e32 v240, v240, v93
	v_add_f32_e32 v241, v241, v110
	v_add_f32_e32 v240, v240, v94
	v_add_f32_e32 v241, v241, v111
	v_add_f32_e32 v240, v240, v95
	v_add_f32_e32 v241, v241, v112
	v_add_f32_e32 v240, v240, v96
	v_add_f32_e32 v241, v241, v97
	v_add_u32_e32 v118, s91, v131
	v_cvt_pk_bf16_f32 v82, v98, v82
	v_cvt_pk_bf16_f32 v83, v83, v84
	v_cvt_pk_bf16_f32 v84, v85, v86
	v_cvt_pk_bf16_f32 v85, v87, v88
	v_cvt_pk_bf16_f32 v86, v89, v90
	v_cvt_pk_bf16_f32 v87, v91, v92
	v_cvt_pk_bf16_f32 v88, v93, v94
	v_cvt_pk_bf16_f32 v89, v95, v96
	v_cvt_pk_bf16_f32 v90, v114, v99
	v_cvt_pk_bf16_f32 v91, v100, v101
	v_cvt_pk_bf16_f32 v92, v102, v103
	v_cvt_pk_bf16_f32 v93, v104, v105
	v_cvt_pk_bf16_f32 v94, v106, v107
	v_cvt_pk_bf16_f32 v95, v108, v109
	v_cvt_pk_bf16_f32 v96, v110, v111
	v_cvt_pk_bf16_f32 v97, v112, v97
	ds_read_b64_tr_b16 v[98:99], v118
	ds_read_b64_tr_b16 v[100:101], v118 offset:2048
	ds_read_b64_tr_b16 v[102:103], v118 offset:4096
	ds_read_b64_tr_b16 v[104:105], v118 offset:6144
	ds_read_b64_tr_b16 v[106:107], v118 offset:8192
	ds_read_b64_tr_b16 v[108:109], v118 offset:10240
	ds_read_b64_tr_b16 v[110:111], v118 offset:12288
	ds_read_b64_tr_b16 v[112:113], v118 offset:14336
	s_waitcnt lgkmcnt(0)
	s_barrier
; __device__ __forceinline__ int crow(int r, int hi) { return (r & 3) + 8 * (r >> 2) + 4 * hi; }
; #define ATT_BAR() do { ATT_SBAR(); asm volatile("s_barrier" ::: "memory"); ATT_SBAR(); } while (0)
; __device__ __forceinline__ unsigned f2bf(float f) { unsigned u = __builtin_bit_cast(unsigned, f); return (u + 0x7fffu + ((u >> 16) & 1u)) >> 16; }
;     ...
;   ATT_XSECTION(false);
;   ATT_BAR();
;   if (grp == 0) ATT_BAR();
; #pragma unroll
;   for (int r = 0; r < 16; ++r) rli[r] = __builtin_amdgcn_rcpf(lacc[r]);
;     ...
;     att::bf16* Ow = Obase + ((size_t)b * SEQ + (size_t)qb * 256 + wave_ * 32) * 2048 + h * 128;
; #pragma unroll
;     for (int r = 0; r < 16; ++r) { const int orow = crow(r, hi);
; #pragma unroll
;         for (int d0 = 0; d0 < 4; ++d0) Ow[(size_t)orow * 2048 + d0 * 32 + r32] = (att::bf16)f2bf(o[d0][r] * rli[r]); }
	s_setprio 2
	s_waitcnt lgkmcnt(6)
	v_mfma_f32_32x32x16_bf16 v[18:33], v[82:85], v[98:101], v[18:33]
	ds_read_b64_tr_b16 v[114:115], v118 offset:512
	ds_read_b64_tr_b16 v[116:117], v118 offset:2560
	s_waitcnt lgkmcnt(6)
	v_mfma_f32_32x32x16_bf16 v[18:33], v[86:89], v[102:105], v[18:33]
	ds_read_b64_tr_b16 v[98:99], v118 offset:4608
	ds_read_b64_tr_b16 v[100:101], v118 offset:6656
	s_waitcnt lgkmcnt(6)
	v_mfma_f32_32x32x16_bf16 v[18:33], v[90:93], v[106:109], v[18:33]
	ds_read_b64_tr_b16 v[102:103], v118 offset:8704
	ds_read_b64_tr_b16 v[104:105], v118 offset:10752
	s_waitcnt lgkmcnt(6)
	v_mfma_f32_32x32x16_bf16 v[18:33], v[94:97], v[110:113], v[18:33]
	ds_read_b64_tr_b16 v[106:107], v118 offset:12800
	ds_read_b64_tr_b16 v[108:109], v118 offset:14848
	s_waitcnt lgkmcnt(6)
	v_mfma_f32_32x32x16_bf16 v[34:49], v[82:85], v[114:117], v[34:49]
	ds_read_b64_tr_b16 v[110:111], v118 offset:1024
	ds_read_b64_tr_b16 v[112:113], v118 offset:3072
	s_waitcnt lgkmcnt(6)
	v_mfma_f32_32x32x16_bf16 v[34:49], v[86:89], v[98:101], v[34:49]
	ds_read_b64_tr_b16 v[114:115], v118 offset:5120
	ds_read_b64_tr_b16 v[116:117], v118 offset:7168
	s_waitcnt lgkmcnt(6)
	v_mfma_f32_32x32x16_bf16 v[34:49], v[90:93], v[102:105], v[34:49]
	ds_read_b64_tr_b16 v[98:99], v118 offset:9216
	ds_read_b64_tr_b16 v[100:101], v118 offset:11264
	s_waitcnt lgkmcnt(6)
	v_mfma_f32_32x32x16_bf16 v[34:49], v[94:97], v[106:109], v[34:49]
	ds_read_b64_tr_b16 v[102:103], v118 offset:13312
	ds_read_b64_tr_b16 v[104:105], v118 offset:15360
	s_waitcnt lgkmcnt(6)
	v_mfma_f32_32x32x16_bf16 v[50:65], v[82:85], v[110:113], v[50:65]
	ds_read_b64_tr_b16 v[106:107], v118 offset:1536
	ds_read_b64_tr_b16 v[108:109], v118 offset:3584
	s_waitcnt lgkmcnt(6)
	v_mfma_f32_32x32x16_bf16 v[50:65], v[86:89], v[114:117], v[50:65]
	ds_read_b64_tr_b16 v[110:111], v118 offset:5632
	ds_read_b64_tr_b16 v[112:113], v118 offset:7680
	s_waitcnt lgkmcnt(6)
	v_mfma_f32_32x32x16_bf16 v[50:65], v[90:93], v[98:101], v[50:65]
	ds_read_b64_tr_b16 v[114:115], v118 offset:9728
	ds_read_b64_tr_b16 v[116:117], v118 offset:11776
	s_waitcnt lgkmcnt(6)
	v_mfma_f32_32x32x16_bf16 v[50:65], v[94:97], v[102:105], v[50:65]
	ds_read_b64_tr_b16 v[98:99], v118 offset:13824
	ds_read_b64_tr_b16 v[100:101], v118 offset:15872
	s_waitcnt lgkmcnt(6)
	v_mfma_f32_32x32x16_bf16 v[66:81], v[82:85], v[106:109], v[66:81]
	s_waitcnt lgkmcnt(4)
	v_mfma_f32_32x32x16_bf16 v[66:81], v[86:89], v[110:113], v[66:81]
	s_waitcnt lgkmcnt(2)
	v_mfma_f32_32x32x16_bf16 v[66:81], v[90:93], v[114:117], v[66:81]
	s_waitcnt lgkmcnt(0)
	v_mfma_f32_32x32x16_bf16 v[66:81], v[94:97], v[98:101], v[66:81]
	s_setprio 0
	s_barrier
	s_cmpk_gt_u32 s88, 0xff
	s_cbranch_scc1 .LBB0_278
	s_barrier
.LBB0_278:
	v_add_f32_e32 v240, v240, v241
	v_mov_b32_e32 v245, v240
	s_nop 1
	v_permlane32_swap_b32_e32 v245, v240
	s_nop 1
	v_add_f32_e32 v240, v240, v245
	ds_write_b32 v187, v240
	v_add_u32_e32 v245, s90, v184
	s_waitcnt lgkmcnt(0)
	ds_read_b128 v[2:5], v245
	ds_read_b128 v[6:9], v245 offset:32
	ds_read_b128 v[10:13], v245 offset:64
	ds_read_b128 v[14:17], v245 offset:96
	s_waitcnt lgkmcnt(0)
	s_ashr_i32 s4, s89, 1
	s_andn2_b32 s4, s4, 31
	s_ashr_i32 s5, s4, 31
	s_add_u32 s4, s4, s51
	s_addc_u32 s5, s5, 0
	s_lshl_b64 s[4:5], s[4:5], 12
	s_nop 2
	v_rcp_f32_e32 v83, v2
	s_add_u32 s4, s44, s4
	s_addc_u32 s5, s45, s5
	v_and_b32_e32 v82, 31, v211
	s_add_u32 s4, s4, s46
	v_rcp_f32_e32 v85, v4
	s_addc_u32 s5, s5, s47
	v_lshlrev_b32_e32 v184, 1, v82
	v_lshlrev_b32_e32 v4, 9, v211
	v_rcp_f32_e32 v84, v3
	v_rcp_f32_e32 v87, v6
	v_lshl_add_u64 v[2:3], s[4:5], 0, v[184:185]
	v_and_b32_e32 v184, 0x4000, v4
	v_mul_f32_e32 v6, v18, v83
	v_rcp_f32_e32 v88, v7
	v_lshl_add_u64 v[2:3], v[2:3], 0, v[184:185]
	v_bfe_u32 v7, v6, 16, 1
	v_add3_u32 v18, v6, v7, s61
	v_add_co_u32_e32 v6, vcc, s63, v2
	v_rcp_f32_e32 v86, v5
	s_nop 0
	v_addc_co_u32_e32 v7, vcc, 0, v3, vcc
	global_store_short_d16_hi v[6:7], v18, off offset:-4096
	v_mul_f32_e32 v18, v34, v83
	v_bfe_u32 v34, v18, 16, 1
	v_lshl_add_u64 v[4:5], v[2:3], 0, s[38:39]
	v_add3_u32 v18, v18, v34, s61
	global_store_short_d16_hi v[4:5], v18, off offset:64
	v_mul_f32_e32 v18, v50, v83
	v_bfe_u32 v34, v18, 16, 1
	v_add3_u32 v18, v18, v34, s61
	global_store_short_d16_hi v[4:5], v18, off offset:128
	v_mul_f32_e32 v18, v66, v83
	v_bfe_u32 v34, v18, 16, 1
	v_add3_u32 v18, v18, v34, s61
	global_store_short_d16_hi v[4:5], v18, off offset:192
	v_mul_f32_e32 v4, v19, v84
	v_bfe_u32 v5, v4, 16, 1
	v_add3_u32 v4, v4, v5, s61
	global_store_short_d16_hi v[6:7], v4, off
	v_mul_f32_e32 v4, v35, v84
	v_bfe_u32 v5, v4, 16, 1
	v_add3_u32 v4, v4, v5, s61
	global_store_short_d16_hi v[6:7], v4, off offset:64
	v_mul_f32_e32 v4, v51, v84
	v_bfe_u32 v5, v4, 16, 1
	v_add3_u32 v4, v4, v5, s61
	global_store_short_d16_hi v[6:7], v4, off offset:128
	v_mul_f32_e32 v4, v67, v84
	v_bfe_u32 v5, v4, 16, 1
	v_add3_u32 v4, v4, v5, s61
	global_store_short_d16_hi v[6:7], v4, off offset:192
	v_mul_f32_e32 v4, v20, v85
	v_bfe_u32 v5, v4, 16, 1
	v_add3_u32 v18, v4, v5, s61
	v_add_co_u32_e32 v4, vcc, s64, v2
	v_rcp_f32_e32 v8, v8
	s_nop 0
	v_addc_co_u32_e32 v5, vcc, 0, v3, vcc
	v_add_co_u32_e32 v6, vcc, s65, v2
	v_rcp_f32_e32 v9, v9
	s_nop 0
	v_addc_co_u32_e32 v7, vcc, 0, v3, vcc
	global_store_short_d16_hi v[6:7], v18, off offset:-4096
	v_mul_f32_e32 v18, v36, v85
	v_bfe_u32 v19, v18, 16, 1
	v_add3_u32 v18, v18, v19, s61
	global_store_short_d16_hi v[4:5], v18, off offset:64
	v_mul_f32_e32 v18, v52, v85
	v_bfe_u32 v19, v18, 16, 1
	v_add3_u32 v18, v18, v19, s61
	global_store_short_d16_hi v[4:5], v18, off offset:128
	v_mul_f32_e32 v18, v68, v85
	v_bfe_u32 v19, v18, 16, 1
	v_add3_u32 v18, v18, v19, s61
; __device__ __forceinline__ int crow(int r, int hi) { return (r & 3) + 8 * (r >> 2) + 4 * hi; }
; __device__ __forceinline__ unsigned f2bf(float f) { unsigned u = __builtin_bit_cast(unsigned, f); return (u + 0x7fffu + ((u >> 16) & 1u)) >> 16; }
;     ...
;     att::bf16* Ow = Obase + ((size_t)b * SEQ + (size_t)qb * 256 + wave_ * 32) * 2048 + h * 128;
; #pragma unroll
;     for (int r = 0; r < 16; ++r) { const int orow = crow(r, hi);
; #pragma unroll
;         for (int d0 = 0; d0 < 4; ++d0) Ow[(size_t)orow * 2048 + d0 * 32 + r32] = (att::bf16)f2bf(o[d0][r] * rli[r]); }
	global_store_short_d16_hi v[4:5], v18, off offset:192
	v_mul_f32_e32 v4, v21, v86
	v_bfe_u32 v5, v4, 16, 1
	v_add3_u32 v4, v4, v5, s61
	global_store_short_d16_hi v[6:7], v4, off
	v_mul_f32_e32 v4, v37, v86
	v_bfe_u32 v5, v4, 16, 1
	v_add3_u32 v4, v4, v5, s61
	global_store_short_d16_hi v[6:7], v4, off offset:64
	v_mul_f32_e32 v4, v53, v86
	v_bfe_u32 v5, v4, 16, 1
	v_add3_u32 v4, v4, v5, s61
	global_store_short_d16_hi v[6:7], v4, off offset:128
	v_mul_f32_e32 v4, v69, v86
	v_bfe_u32 v5, v4, 16, 1
	v_add3_u32 v4, v4, v5, s61
	global_store_short_d16_hi v[6:7], v4, off offset:192
	v_mul_f32_e32 v4, v22, v87
	v_bfe_u32 v5, v4, 16, 1
	v_add3_u32 v18, v4, v5, s61
	v_add_co_u32_e32 v4, vcc, s66, v2
	v_rcp_f32_e32 v10, v10
	s_nop 0
	v_addc_co_u32_e32 v5, vcc, 0, v3, vcc
	v_add_co_u32_e32 v6, vcc, s67, v2
	v_rcp_f32_e32 v11, v11
	s_nop 0
	v_addc_co_u32_e32 v7, vcc, 0, v3, vcc
	global_store_short_d16_hi v[6:7], v18, off offset:-4096
	v_mul_f32_e32 v18, v38, v87
	v_bfe_u32 v19, v18, 16, 1
	v_add3_u32 v18, v18, v19, s61
	global_store_short_d16_hi v[4:5], v18, off offset:64
	v_mul_f32_e32 v18, v54, v87
	v_bfe_u32 v19, v18, 16, 1
	v_add3_u32 v18, v18, v19, s61
	global_store_short_d16_hi v[4:5], v18, off offset:128
	v_mul_f32_e32 v18, v70, v87
	v_bfe_u32 v19, v18, 16, 1
	v_add3_u32 v18, v18, v19, s61
	global_store_short_d16_hi v[4:5], v18, off offset:192
	v_mul_f32_e32 v4, v23, v88
	v_bfe_u32 v5, v4, 16, 1
	v_add3_u32 v4, v4, v5, s61
	global_store_short_d16_hi v[6:7], v4, off
	v_mul_f32_e32 v4, v39, v88
	v_bfe_u32 v5, v4, 16, 1
	v_add3_u32 v4, v4, v5, s61
	global_store_short_d16_hi v[6:7], v4, off offset:64
	v_mul_f32_e32 v4, v55, v88
	v_bfe_u32 v5, v4, 16, 1
	v_add3_u32 v4, v4, v5, s61
	global_store_short_d16_hi v[6:7], v4, off offset:128
	v_mul_f32_e32 v4, v71, v88
	v_bfe_u32 v5, v4, 16, 1
	v_add3_u32 v4, v4, v5, s61
	global_store_short_d16_hi v[6:7], v4, off offset:192
	v_mul_f32_e32 v4, v24, v8
	v_bfe_u32 v5, v4, 16, 1
	v_add3_u32 v18, v4, v5, s61
	v_add_co_u32_e32 v4, vcc, s68, v2
	v_rcp_f32_e32 v12, v12
	s_nop 0
	v_addc_co_u32_e32 v5, vcc, 0, v3, vcc
	v_add_co_u32_e32 v6, vcc, s69, v2
	v_rcp_f32_e32 v13, v13
	s_nop 0
	v_addc_co_u32_e32 v7, vcc, 0, v3, vcc
	global_store_short_d16_hi v[6:7], v18, off offset:-4096
	v_mul_f32_e32 v18, v40, v8
	v_bfe_u32 v19, v18, 16, 1
	v_add3_u32 v18, v18, v19, s61
	global_store_short_d16_hi v[4:5], v18, off offset:64
	v_mul_f32_e32 v18, v56, v8
	v_bfe_u32 v19, v18, 16, 1
	v_add3_u32 v18, v18, v19, s61
	v_mul_f32_e32 v8, v72, v8
	global_store_short_d16_hi v[4:5], v18, off offset:128
	v_bfe_u32 v18, v8, 16, 1
	v_add3_u32 v8, v8, v18, s61
	global_store_short_d16_hi v[4:5], v8, off offset:192
	v_mul_f32_e32 v4, v25, v9
	v_bfe_u32 v5, v4, 16, 1
	v_add3_u32 v4, v4, v5, s61
	global_store_short_d16_hi v[6:7], v4, off
	v_mul_f32_e32 v4, v41, v9
	v_bfe_u32 v5, v4, 16, 1
	v_add3_u32 v4, v4, v5, s61
	global_store_short_d16_hi v[6:7], v4, off offset:64
	v_mul_f32_e32 v4, v57, v9
	v_bfe_u32 v5, v4, 16, 1
	v_add3_u32 v4, v4, v5, s61
	global_store_short_d16_hi v[6:7], v4, off offset:128
	v_mul_f32_e32 v4, v73, v9
	v_bfe_u32 v5, v4, 16, 1
	v_add3_u32 v4, v4, v5, s61
	global_store_short_d16_hi v[6:7], v4, off offset:192
	v_mul_f32_e32 v4, v26, v10
	v_bfe_u32 v5, v4, 16, 1
	v_add3_u32 v8, v4, v5, s61
	v_add_co_u32_e32 v4, vcc, s74, v2
	v_rcp_f32_e32 v14, v14
	s_nop 0
	v_addc_co_u32_e32 v5, vcc, 0, v3, vcc
	v_add_co_u32_e32 v6, vcc, s75, v2
	v_rcp_f32_e32 v15, v15
	s_nop 0
	v_addc_co_u32_e32 v7, vcc, 0, v3, vcc
	global_store_short_d16_hi v[6:7], v8, off offset:-4096
	v_mul_f32_e32 v8, v42, v10
	v_bfe_u32 v9, v8, 16, 1
	v_add3_u32 v8, v8, v9, s61
	global_store_short_d16_hi v[4:5], v8, off offset:64
	v_mul_f32_e32 v8, v58, v10
	v_bfe_u32 v9, v8, 16, 1
	v_add3_u32 v8, v8, v9, s61
	global_store_short_d16_hi v[4:5], v8, off offset:128
	v_mul_f32_e32 v8, v74, v10
	v_bfe_u32 v9, v8, 16, 1
	v_add3_u32 v8, v8, v9, s61
	global_store_short_d16_hi v[4:5], v8, off offset:192
	v_mul_f32_e32 v4, v27, v11
	v_bfe_u32 v5, v4, 16, 1
	v_add3_u32 v4, v4, v5, s61
	global_store_short_d16_hi v[6:7], v4, off
	v_mul_f32_e32 v4, v43, v11
	v_bfe_u32 v5, v4, 16, 1
	v_add3_u32 v4, v4, v5, s61
; __device__ __forceinline__ int crow(int r, int hi) { return (r & 3) + 8 * (r >> 2) + 4 * hi; }
; __device__ __forceinline__ unsigned f2bf(float f) { unsigned u = __builtin_bit_cast(unsigned, f); return (u + 0x7fffu + ((u >> 16) & 1u)) >> 16; }
;     ...
;     att::bf16* Ow = Obase + ((size_t)b * SEQ + (size_t)qb * 256 + wave_ * 32) * 2048 + h * 128;
; #pragma unroll
;     for (int r = 0; r < 16; ++r) { const int orow = crow(r, hi);
; #pragma unroll
;         for (int d0 = 0; d0 < 4; ++d0) Ow[(size_t)orow * 2048 + d0 * 32 + r32] = (att::bf16)f2bf(o[d0][r] * rli[r]); }
	global_store_short_d16_hi v[6:7], v4, off offset:64
	v_mul_f32_e32 v4, v59, v11
	v_bfe_u32 v5, v4, 16, 1
	v_add3_u32 v4, v4, v5, s61
	global_store_short_d16_hi v[6:7], v4, off offset:128
	v_mul_f32_e32 v4, v75, v11
	v_bfe_u32 v5, v4, 16, 1
	v_add3_u32 v4, v4, v5, s61
	global_store_short_d16_hi v[6:7], v4, off offset:192
	v_mul_f32_e32 v4, v28, v12
	v_bfe_u32 v5, v4, 16, 1
	v_add3_u32 v8, v4, v5, s61
	v_add_co_u32_e32 v4, vcc, s76, v2
	v_rcp_f32_e32 v16, v16
	s_nop 0
	v_addc_co_u32_e32 v5, vcc, 0, v3, vcc
	v_add_co_u32_e32 v6, vcc, s77, v2
	v_rcp_f32_e32 v17, v17
	s_nop 0
	v_addc_co_u32_e32 v7, vcc, 0, v3, vcc
	global_store_short_d16_hi v[6:7], v8, off offset:-4096
	v_mul_f32_e32 v8, v44, v12
	v_bfe_u32 v9, v8, 16, 1
	v_add3_u32 v8, v8, v9, s61
	global_store_short_d16_hi v[4:5], v8, off offset:64
	v_mul_f32_e32 v8, v60, v12
	v_bfe_u32 v9, v8, 16, 1
	v_add3_u32 v8, v8, v9, s61
	global_store_short_d16_hi v[4:5], v8, off offset:128
	v_mul_f32_e32 v8, v76, v12
	v_bfe_u32 v9, v8, 16, 1
	v_add3_u32 v8, v8, v9, s61
	global_store_short_d16_hi v[4:5], v8, off offset:192
	v_mul_f32_e32 v4, v29, v13
	v_bfe_u32 v5, v4, 16, 1
	v_add3_u32 v4, v4, v5, s61
	global_store_short_d16_hi v[6:7], v4, off
	v_mul_f32_e32 v4, v45, v13
	v_bfe_u32 v5, v4, 16, 1
	v_add3_u32 v4, v4, v5, s61
	global_store_short_d16_hi v[6:7], v4, off offset:64
	v_mul_f32_e32 v4, v61, v13
	v_bfe_u32 v5, v4, 16, 1
	v_add3_u32 v4, v4, v5, s61
	global_store_short_d16_hi v[6:7], v4, off offset:128
	v_mul_f32_e32 v4, v77, v13
	v_bfe_u32 v5, v4, 16, 1
	v_add3_u32 v4, v4, v5, s61
	global_store_short_d16_hi v[6:7], v4, off offset:192
	v_mul_f32_e32 v4, v30, v14
	v_bfe_u32 v5, v4, 16, 1
	v_add3_u32 v8, v4, v5, s61
	v_add_co_u32_e32 v4, vcc, s78, v2
	s_nop 1
	v_addc_co_u32_e32 v5, vcc, 0, v3, vcc
	v_add_co_u32_e32 v6, vcc, s79, v2
	s_nop 1
	v_addc_co_u32_e32 v7, vcc, 0, v3, vcc
	global_store_short_d16_hi v[6:7], v8, off offset:-4096
	v_mul_f32_e32 v8, v46, v14
	v_bfe_u32 v9, v8, 16, 1
	v_add3_u32 v8, v8, v9, s61
	global_store_short_d16_hi v[4:5], v8, off offset:64
	v_mul_f32_e32 v8, v62, v14
	v_bfe_u32 v9, v8, 16, 1
	v_add3_u32 v8, v8, v9, s61
	global_store_short_d16_hi v[4:5], v8, off offset:128
	v_mul_f32_e32 v8, v78, v14
	v_bfe_u32 v9, v8, 16, 1
	v_add3_u32 v8, v8, v9, s61
	global_store_short_d16_hi v[4:5], v8, off offset:192
	v_mul_f32_e32 v4, v31, v15
	v_bfe_u32 v5, v4, 16, 1
	v_add3_u32 v4, v4, v5, s61
	global_store_short_d16_hi v[6:7], v4, off
	v_mul_f32_e32 v4, v47, v15
	v_bfe_u32 v5, v4, 16, 1
	v_add3_u32 v4, v4, v5, s61
	global_store_short_d16_hi v[6:7], v4, off offset:64
	v_mul_f32_e32 v4, v63, v15
	v_bfe_u32 v5, v4, 16, 1
	v_add3_u32 v4, v4, v5, s61
	global_store_short_d16_hi v[6:7], v4, off offset:128
	v_mul_f32_e32 v4, v79, v15
	v_bfe_u32 v5, v4, 16, 1
	v_add3_u32 v4, v4, v5, s61
	global_store_short_d16_hi v[6:7], v4, off offset:192
	v_mul_f32_e32 v4, v32, v16
	v_bfe_u32 v5, v4, 16, 1
	v_add3_u32 v6, v4, v5, s61
	v_add_co_u32_e32 v4, vcc, s80, v2
	s_nop 1
	v_addc_co_u32_e32 v5, vcc, 0, v3, vcc
	v_add_co_u32_e32 v2, vcc, s81, v2
	s_nop 1
	v_addc_co_u32_e32 v3, vcc, 0, v3, vcc
	global_store_short_d16_hi v[2:3], v6, off offset:-4096
	v_mul_f32_e32 v6, v48, v16
	v_bfe_u32 v7, v6, 16, 1
	v_add3_u32 v6, v6, v7, s61
	global_store_short_d16_hi v[4:5], v6, off offset:64
	v_mul_f32_e32 v6, v64, v16
	v_bfe_u32 v7, v6, 16, 1
	v_add3_u32 v6, v6, v7, s61
	global_store_short_d16_hi v[4:5], v6, off offset:128
	v_mul_f32_e32 v6, v80, v16
	v_bfe_u32 v7, v6, 16, 1
	v_add3_u32 v6, v6, v7, s61
	global_store_short_d16_hi v[4:5], v6, off offset:192
	v_mul_f32_e32 v4, v33, v17
	v_bfe_u32 v5, v4, 16, 1
	v_add3_u32 v4, v4, v5, s61
	global_store_short_d16_hi v[2:3], v4, off
	v_mul_f32_e32 v4, v49, v17
	v_bfe_u32 v5, v4, 16, 1
	v_add3_u32 v4, v4, v5, s61
	global_store_short_d16_hi v[2:3], v4, off offset:64
	v_mul_f32_e32 v4, v65, v17
	v_bfe_u32 v5, v4, 16, 1
	v_add3_u32 v4, v4, v5, s61
	global_store_short_d16_hi v[2:3], v4, off offset:128
	v_mul_f32_e32 v4, v81, v17
	v_bfe_u32 v5, v4, 16, 1
	v_add3_u32 v4, v4, v5, s61
	global_store_short_d16_hi v[2:3], v4, off offset:192
	s_cmp_lt_i32 s49, 4
	s_cbranch_scc1 .LBB0_260

; __device__ __forceinline__ float softmax_shift(f32x16& p0, f32x16& p1, f32x16& negm, float pmax, bool first) {
;   asm volatile("s_nop 4" ::: "memory");
;   { auto rr = __builtin_amdgcn_permlane32_swap(__float_as_uint(pmax), __float_as_uint(pmax), false, false);
;     pmax = fmaxf(__uint_as_float(rr[0]), __uint_as_float(rr[1])); }
;   const float delta = first ? pmax : fmaxf(pmax, 0.f);
; #pragma unroll
;   for (int r = 0; r < 16; ++r) { p0[r] -= delta; p1[r] -= delta; negm[r] -= delta; }
;   return first ? 1.f : __builtin_amdgcn_exp2f(-delta);
; }
.LBB0_309:
	v_mov_b32_e32 v192, v191
	s_nop 1
	v_permlane32_swap_b32_e32 v191, v192
	v_max3_f32 v191, v191, v192, 0
	v_exp_f32_e64 v192, -v191
	s_nop 4
	s_nop 0
	v_cmp_gt_f32_e32 vcc, 1.0, v192
	s_cbranch_vccz .LBB0_313
	v_mul_f32_e32 v240, v192, v240
	v_mul_f32_e32 v241, v192, v241
	s_and_saveexec_b64 s[8:9], s[4:5]
	ds_write_b32 v187, v192
	s_or_b64 exec, exec, s[8:9]
	s_waitcnt lgkmcnt(0)
	v_add_u32_e32 v200, s90, v184
	ds_read_b128 v[192:195], v200 offset:96
	ds_read_b128 v[196:199], v200 offset:64
	ds_read_b128 v[212:215], v200 offset:32
	ds_read_b128 v[216:219], v200
	s_waitcnt lgkmcnt(3)
	v_pk_mul_f32 v[30:31], v[30:31], v[192:193]
	s_waitcnt lgkmcnt(2)
	v_pk_mul_f32 v[26:27], v[26:27], v[196:197]
	s_waitcnt lgkmcnt(1)
	v_pk_mul_f32 v[22:23], v[22:23], v[212:213]
	v_pk_mul_f32 v[32:33], v[32:33], v[194:195]
	v_pk_mul_f32 v[28:29], v[28:29], v[198:199]
	v_pk_mul_f32 v[24:25], v[24:25], v[214:215]
	s_waitcnt lgkmcnt(0)
	v_pk_mul_f32 v[20:21], v[20:21], v[218:219]
	v_pk_mul_f32 v[18:19], v[18:19], v[216:217]
	v_pk_mul_f32 v[46:47], v[46:47], v[192:193]
	v_pk_mul_f32 v[42:43], v[42:43], v[196:197]
	v_pk_mul_f32 v[38:39], v[38:39], v[212:213]
	v_pk_mul_f32 v[48:49], v[48:49], v[194:195]
	v_pk_mul_f32 v[44:45], v[44:45], v[198:199]
	v_pk_mul_f32 v[40:41], v[40:41], v[214:215]
	v_pk_mul_f32 v[36:37], v[36:37], v[218:219]
	v_pk_mul_f32 v[34:35], v[34:35], v[216:217]
	v_pk_mul_f32 v[62:63], v[62:63], v[192:193]
	v_pk_mul_f32 v[58:59], v[58:59], v[196:197]
	v_pk_mul_f32 v[54:55], v[54:55], v[212:213]
	v_pk_mul_f32 v[64:65], v[64:65], v[194:195]
	v_pk_mul_f32 v[60:61], v[60:61], v[198:199]
	v_pk_mul_f32 v[56:57], v[56:57], v[214:215]
	v_pk_mul_f32 v[52:53], v[52:53], v[218:219]
	v_pk_mul_f32 v[50:51], v[50:51], v[216:217]
	v_pk_mul_f32 v[78:79], v[78:79], v[192:193]
	v_pk_mul_f32 v[74:75], v[74:75], v[196:197]
	v_pk_mul_f32 v[70:71], v[70:71], v[212:213]
	v_pk_mul_f32 v[80:81], v[80:81], v[194:195]
	v_pk_mul_f32 v[76:77], v[76:77], v[198:199]
	v_pk_mul_f32 v[72:73], v[72:73], v[214:215]
	v_pk_mul_f32 v[68:69], v[68:69], v[218:219]
	v_pk_mul_f32 v[66:67], v[66:67], v[216:217]

; __device__ __forceinline__ float softmax_shift(f32x16& p0, f32x16& p1, f32x16& negm, float pmax, bool first) {
;   asm volatile("s_nop 4" ::: "memory");
;   { auto rr = __builtin_amdgcn_permlane32_swap(__float_as_uint(pmax), __float_as_uint(pmax), false, false);
;     pmax = fmaxf(__uint_as_float(rr[0]), __uint_as_float(rr[1])); }
;   const float delta = first ? pmax : fmaxf(pmax, 0.f);
; #pragma unroll
;   for (int r = 0; r < 16; ++r) { p0[r] -= delta; p1[r] -= delta; negm[r] -= delta; }
;   return first ? 1.f : __builtin_amdgcn_exp2f(-delta);
; }
.LBB0_314:
	v_mov_b32_e32 v115, v114
	s_nop 1
	v_permlane32_swap_b32_e32 v114, v115
	v_max3_f32 v114, v114, v115, 0
	v_exp_f32_e64 v115, -v114
	s_nop 4
	s_nop 0
	v_cmp_gt_f32_e32 vcc, 1.0, v115
	s_cbranch_vccz .LBB0_318
	v_mul_f32_e32 v240, v115, v240
	v_mul_f32_e32 v241, v115, v241
	s_and_saveexec_b64 s[8:9], s[4:5]
	ds_write_b32 v187, v115
	s_or_b64 exec, exec, s[8:9]
	s_waitcnt lgkmcnt(0)
	v_add_u32_e32 v115, s90, v184
	ds_read_b128 v[116:119], v115 offset:96
	ds_read_b128 v[120:123], v115 offset:64
	ds_read_b128 v[124:127], v115 offset:32
	ds_read_b128 v[136:139], v115
	s_waitcnt lgkmcnt(3)
	v_pk_mul_f32 v[30:31], v[30:31], v[116:117]
	s_waitcnt lgkmcnt(2)
	v_pk_mul_f32 v[26:27], v[26:27], v[120:121]
	s_waitcnt lgkmcnt(1)
	v_pk_mul_f32 v[22:23], v[22:23], v[124:125]
	v_pk_mul_f32 v[32:33], v[32:33], v[118:119]
	v_pk_mul_f32 v[28:29], v[28:29], v[122:123]
	v_pk_mul_f32 v[24:25], v[24:25], v[126:127]
	s_waitcnt lgkmcnt(0)
	v_pk_mul_f32 v[20:21], v[20:21], v[138:139]
	v_pk_mul_f32 v[18:19], v[18:19], v[136:137]
	v_pk_mul_f32 v[46:47], v[46:47], v[116:117]
	v_pk_mul_f32 v[42:43], v[42:43], v[120:121]
	v_pk_mul_f32 v[38:39], v[38:39], v[124:125]
	v_pk_mul_f32 v[48:49], v[48:49], v[118:119]
	v_pk_mul_f32 v[44:45], v[44:45], v[122:123]
	v_pk_mul_f32 v[40:41], v[40:41], v[126:127]
	v_pk_mul_f32 v[36:37], v[36:37], v[138:139]
	v_pk_mul_f32 v[34:35], v[34:35], v[136:137]
	v_pk_mul_f32 v[62:63], v[62:63], v[116:117]
	v_pk_mul_f32 v[58:59], v[58:59], v[120:121]
	v_pk_mul_f32 v[54:55], v[54:55], v[124:125]
	v_pk_mul_f32 v[64:65], v[64:65], v[118:119]
	v_pk_mul_f32 v[60:61], v[60:61], v[122:123]
	v_pk_mul_f32 v[56:57], v[56:57], v[126:127]
	v_pk_mul_f32 v[52:53], v[52:53], v[138:139]
	v_pk_mul_f32 v[50:51], v[50:51], v[136:137]
	v_pk_mul_f32 v[78:79], v[78:79], v[116:117]
	v_pk_mul_f32 v[74:75], v[74:75], v[120:121]
	v_pk_mul_f32 v[70:71], v[70:71], v[124:125]
	v_pk_mul_f32 v[80:81], v[80:81], v[118:119]
	v_pk_mul_f32 v[76:77], v[76:77], v[122:123]
	v_pk_mul_f32 v[72:73], v[72:73], v[126:127]
	v_pk_mul_f32 v[68:69], v[68:69], v[138:139]
	v_pk_mul_f32 v[66:67], v[66:67], v[136:137]
